# whole attention unit code (prologue, band, drain, epilogue as well as the main loop): 8-byte instructions on 8-byte boundaries
# speedup vs baseline: 1.0054x; 1.0054x over previous
.LBB0_715:
	s_cmp_lt_i32 s24, 1
	s_cbranch_scc1 .LBB0_806
	s_add_u32 s25, s70, 0x1ee00000
	s_addc_u32 s26, s71, 0
	s_mov_b32 s27, 0
	s_mov_b32 s28, -1
	v_readlane_b32 s50, v254, 49
	s_branch .LBB0_718
	s_nop 0
.LBB0_717:
	s_or_b64 exec, exec, s[2:3]
	s_waitcnt lgkmcnt(0)
	ds_read_b128 v[32:35], v219 offset:49280
	ds_read_b128 v[36:39], v219 offset:49312
	s_lshl_b32 s2, s29, 12
	s_add_i32 s2, s2, 0
	v_lshlrev_b32_e32 v48, 1, v214
	s_waitcnt lgkmcnt(1)
	v_rcp_f32_e32 v40, v32
	v_rcp_f32_e32 v41, v33
	v_lshlrev_b32_e32 v49, 9, v215
	s_nop 0
	v_add3_u32 v48, s2, v48, v49
	v_mul_f32_e64 v0, v0, v40
	v_cvt_pk_bf16_f32 v0, v0, s0
	v_rcp_f32_e32 v42, v34
	v_rcp_f32_e32 v43, v35
	s_waitcnt lgkmcnt(0)
	v_rcp_f32_e32 v44, v36
	ds_read_b128 v[32:35], v219 offset:49344
	v_rcp_f32_e32 v45, v37
	v_rcp_f32_e32 v46, v38
	v_rcp_f32_e32 v47, v39
	s_nop 0
	ds_read_b128 v[36:39], v219 offset:49376
	ds_write_b16 v48, v0 offset:51264
	v_mul_f32_e64 v0, v17, v41
	v_cvt_pk_bf16_f32 v0, v0, s0
	ds_write_b16 v48, v0 offset:51328
	v_mul_f32_e64 v0, v1, v41
	v_cvt_pk_bf16_f32 v0, v0, s0
	ds_write_b16 v48, v0 offset:51392
	v_mul_f32_e64 v0, v18, v42
	v_cvt_pk_bf16_f32 v0, v0, s0
	ds_write_b16 v48, v0 offset:51456
	v_mul_f32_e64 v0, v2, v42
	v_cvt_pk_bf16_f32 v0, v0, s0
	ds_write_b16 v48, v0 offset:51520
	v_mul_f32_e64 v0, v19, v43
	v_cvt_pk_bf16_f32 v0, v0, s0
	ds_write_b16 v48, v0 offset:51584
	v_mul_f32_e64 v0, v3, v43
	v_cvt_pk_bf16_f32 v0, v0, s0
	ds_write_b16 v48, v0 offset:51648
	v_mul_f32_e64 v0, v20, v44
	v_cvt_pk_bf16_f32 v0, v0, s0
	ds_write_b16 v48, v0 offset:52224
	v_mul_f32_e64 v0, v4, v44
	v_cvt_pk_bf16_f32 v0, v0, s0
	ds_write_b16 v48, v0 offset:52288
	v_mul_f32_e64 v0, v21, v45
	v_cvt_pk_bf16_f32 v0, v0, s0
	ds_write_b16 v48, v0 offset:52352
	v_mul_f32_e64 v0, v5, v45
	v_cvt_pk_bf16_f32 v0, v0, s0
	ds_write_b16 v48, v0 offset:52416
	v_mul_f32_e64 v0, v22, v46
	v_cvt_pk_bf16_f32 v0, v0, s0
	ds_write_b16 v48, v0 offset:52480
	v_mul_f32_e64 v0, v6, v46
	v_cvt_pk_bf16_f32 v0, v0, s0
	s_waitcnt lgkmcnt(13)
	v_rcp_f32_e32 v32, v32
	ds_write_b16 v48, v0 offset:52544
	v_mul_f32_e64 v0, v23, v47
	v_cvt_pk_bf16_f32 v0, v0, s0
	ds_write_b16 v48, v0 offset:52608
	v_mul_f32_e64 v0, v7, v47
	v_cvt_pk_bf16_f32 v0, v0, s0
	v_rcp_f32_e32 v33, v33
	s_nop 0
	ds_write_b16 v48, v0 offset:52672
	v_mul_f32_e64 v0, v24, v32
	v_cvt_pk_bf16_f32 v0, v0, s0
	ds_write_b16 v48, v0 offset:53248
	v_mul_f32_e64 v0, v8, v32
	v_cvt_pk_bf16_f32 v0, v0, s0
	v_rcp_f32_e32 v34, v34
	s_nop 0
	ds_write_b16 v48, v0 offset:53312
	v_mul_f32_e64 v0, v25, v33
	v_cvt_pk_bf16_f32 v0, v0, s0
	ds_write_b16 v48, v0 offset:53376
	v_mul_f32_e64 v0, v9, v33
	v_cvt_pk_bf16_f32 v0, v0, s0
	v_rcp_f32_e32 v35, v35
	s_nop 0
	ds_write_b16 v48, v0 offset:53440
	v_mul_f32_e64 v0, v26, v34
	v_cvt_pk_bf16_f32 v0, v0, s0
	ds_write_b16 v48, v0 offset:53504
	v_mul_f32_e64 v0, v10, v34
	v_cvt_pk_bf16_f32 v0, v0, s0
	s_waitcnt lgkmcnt(14)
	v_rcp_f32_e32 v36, v36
	ds_write_b16 v48, v0 offset:53568
	v_mul_f32_e64 v0, v27, v35
	v_cvt_pk_bf16_f32 v0, v0, s0
	ds_write_b16 v48, v0 offset:53632
	v_mul_f32_e64 v0, v11, v35
	v_cvt_pk_bf16_f32 v0, v0, s0
	v_rcp_f32_e32 v37, v37
	s_nop 0
	ds_write_b16 v48, v0 offset:53696
	v_mul_f32_e64 v0, v28, v36
	v_cvt_pk_bf16_f32 v0, v0, s0
	ds_write_b16 v48, v0 offset:54272
	v_mul_f32_e64 v0, v12, v36
	v_cvt_pk_bf16_f32 v0, v0, s0
	v_rcp_f32_e32 v38, v38
	s_nop 0
	ds_write_b16 v48, v0 offset:54336
	v_mul_f32_e64 v0, v29, v37
	v_cvt_pk_bf16_f32 v0, v0, s0
	ds_write_b16 v48, v0 offset:54400
	v_mul_f32_e64 v0, v13, v37
	v_cvt_pk_bf16_f32 v0, v0, s0
	v_rcp_f32_e32 v39, v39
	s_nop 0
	ds_write_b16 v48, v0 offset:54464
	v_mul_f32_e64 v0, v30, v38
	v_cvt_pk_bf16_f32 v0, v0, s0
	ds_write_b16 v48, v0 offset:54528
	v_mul_f32_e64 v0, v14, v38
	v_cvt_pk_bf16_f32 v0, v0, s0
	ds_write_b16 v48, v0 offset:54592
	v_mul_f32_e64 v0, v31, v39
	v_cvt_pk_bf16_f32 v0, v0, s0
	v_mul_f32_e64 v16, v16, v40
	ds_write_b16 v48, v0 offset:54656
	v_mul_f32_e64 v0, v15, v39
	v_cvt_pk_bf16_f32 v16, v16, s0
	v_cvt_pk_bf16_f32 v0, v0, s0
	v_and_b32_e32 v96, 56, v203
	s_nop 0
	ds_write_b16 v48, v16 offset:51200
	ds_write_b16 v48, v0 offset:54720
	v_lshrrev_b32_e32 v12, 3, v199
	s_nop 0
	v_lshl_add_u32 v13, v96, 1, s2
	s_waitcnt lgkmcnt(0)
	s_nop 0
	v_lshl_add_u32 v0, v12, 7, v13
	ds_read_b128 v[0:3], v0 offset:51200
	v_or_b32_e32 v14, 8, v12
	s_nop 0
	v_lshl_add_u32 v4, v14, 7, v13
	ds_read_b128 v[4:7], v4 offset:51200
	s_add_u32 s2, s78, s10
	s_waitcnt lgkmcnt(1)
	v_lshlrev_b32_e32 v10, 16, v0
	s_nop 0
	v_and_b32_e32 v0, 0xffff0000, v0
	v_med3_f32 v10, v10, s82, v229
	v_med3_f32 v11, v0, s82, v229
	v_mov_b32_e64 v0, v97
	v_cvt_pk_fp8_f32 v0, v10, v11
	v_lshlrev_b32_e32 v10, 16, v1
	s_nop 0
	v_and_b32_e32 v1, 0xffff0000, v1
	v_med3_f32 v10, v10, s82, v229
	v_med3_f32 v1, v1, s82, v229
	v_cvt_pk_fp8_f32 v0, v10, v1 op_sel:[0,0,1]
	v_lshlrev_b32_e32 v1, 16, v2
	s_nop 0
	v_and_b32_e32 v2, 0xffff0000, v2
	v_med3_f32 v10, v1, s82, v229
	v_med3_f32 v2, v2, s82, v229
	v_mov_b32_e64 v1, v97
	v_cvt_pk_fp8_f32 v1, v10, v2
	v_lshlrev_b32_e32 v2, 16, v3
	s_nop 0
	v_and_b32_e32 v3, 0xffff0000, v3
	v_med3_f32 v2, v2, s82, v229
	v_med3_f32 v3, v3, s82, v229
	v_cvt_pk_fp8_f32 v1, v2, v3 op_sel:[0,0,1]
	s_addc_u32 s3, s79, s11
	v_or_b32_e32 v10, s8, v12
	v_mov_b32_e64 v11, s9
	v_lshl_add_u64 v[8:9], s[2:3], 0, v[96:97]
	v_lshlrev_b64 v[2:3], 10, v[10:11]
	v_lshl_add_u64 v[2:3], v[8:9], 0, v[2:3]
	global_store_dwordx2 v[2:3], v[0:1], off
	s_waitcnt lgkmcnt(0)
	v_lshlrev_b32_e32 v0, 16, v4
	v_and_b32_e32 v1, 0xffff0000, v4
	v_med3_f32 v0, v0, s82, v229
	v_med3_f32 v1, v1, s82, v229
	v_mov_b32_e64 v4, v97
	v_cvt_pk_fp8_f32 v4, v0, v1
	v_lshlrev_b32_e32 v0, 16, v5
	s_nop 0
	v_and_b32_e32 v1, 0xffff0000, v5
	v_med3_f32 v0, v0, s82, v229
	v_med3_f32 v1, v1, s82, v229
	v_cvt_pk_fp8_f32 v4, v0, v1 op_sel:[0,0,1]
	v_lshlrev_b32_e32 v0, 16, v6
	s_nop 0
	v_and_b32_e32 v1, 0xffff0000, v6
	v_med3_f32 v0, v0, s82, v229
	v_med3_f32 v1, v1, s82, v229
	v_mov_b32_e64 v5, v97
	v_cvt_pk_fp8_f32 v5, v0, v1
	v_lshlrev_b32_e32 v0, 16, v7
	s_nop 0
	v_and_b32_e32 v1, 0xffff0000, v7
	v_med3_f32 v0, v0, s82, v229
	v_med3_f32 v1, v1, s82, v229
	v_or_b32_e32 v10, s8, v14
	s_nop 0
	v_cvt_pk_fp8_f32 v5, v0, v1 op_sel:[0,0,1]
	v_lshlrev_b64 v[0:1], 10, v[10:11]
	v_or_b32_e32 v10, 16, v12
	s_nop 0
	v_lshl_add_u64 v[6:7], v[8:9], 0, v[0:1]
	v_lshl_add_u32 v0, v10, 7, v13
	ds_read_b128 v[0:3], v0 offset:51200
	v_or_b32_e32 v12, 24, v12
	s_nop 0
	global_store_dwordx2 v[6:7], v[4:5], off
	v_lshl_add_u32 v4, v12, 7, v13
	ds_read_b128 v[4:7], v4 offset:51200
	s_waitcnt lgkmcnt(1)
	v_lshlrev_b32_e32 v13, 16, v0
	v_and_b32_e32 v0, 0xffff0000, v0
	v_med3_f32 v13, v13, s82, v229
	v_med3_f32 v14, v0, s82, v229
	v_mov_b32_e64 v0, v97
	v_cvt_pk_fp8_f32 v0, v13, v14
	v_lshlrev_b32_e32 v13, 16, v1
	s_nop 0
	v_and_b32_e32 v1, 0xffff0000, v1
	v_med3_f32 v13, v13, s82, v229
	v_med3_f32 v1, v1, s82, v229
	v_cvt_pk_fp8_f32 v0, v13, v1 op_sel:[0,0,1]
	v_lshlrev_b32_e32 v1, 16, v2
	s_nop 0
	v_and_b32_e32 v2, 0xffff0000, v2
	v_med3_f32 v13, v1, s82, v229
	v_med3_f32 v2, v2, s82, v229
	v_mov_b32_e64 v1, v97
	v_cvt_pk_fp8_f32 v1, v13, v2
	v_lshlrev_b32_e32 v2, 16, v3
	s_nop 0
	v_and_b32_e32 v3, 0xffff0000, v3
	v_med3_f32 v2, v2, s82, v229
	v_med3_f32 v3, v3, s82, v229
	v_cvt_pk_fp8_f32 v1, v2, v3 op_sel:[0,0,1]
	v_or_b32_e32 v10, s8, v10
	s_nop 0
	v_lshlrev_b64 v[2:3], 10, v[10:11]
	v_lshl_add_u64 v[2:3], v[8:9], 0, v[2:3]
	global_store_dwordx2 v[2:3], v[0:1], off
	s_waitcnt lgkmcnt(0)
	v_lshlrev_b32_e32 v0, 16, v4
	v_and_b32_e32 v1, 0xffff0000, v4
	v_med3_f32 v2, v0, s82, v229
	v_med3_f32 v1, v1, s82, v229
	v_mov_b32_e64 v0, v97
	v_cvt_pk_fp8_f32 v0, v2, v1
	v_lshlrev_b32_e32 v1, 16, v5
	s_nop 0
	v_and_b32_e32 v2, 0xffff0000, v5
	v_med3_f32 v1, v1, s82, v229
	v_med3_f32 v2, v2, s82, v229
	v_cvt_pk_fp8_f32 v0, v1, v2 op_sel:[0,0,1]
	v_lshlrev_b32_e32 v1, 16, v6
	s_nop 0
	v_and_b32_e32 v2, 0xffff0000, v6
	v_med3_f32 v3, v1, s82, v229
	v_med3_f32 v2, v2, s82, v229
	v_mov_b32_e64 v1, v97
	v_cvt_pk_fp8_f32 v1, v3, v2
	v_lshlrev_b32_e32 v2, 16, v7
	s_nop 0
	v_and_b32_e32 v3, 0xffff0000, v7
	v_med3_f32 v2, v2, s82, v229
	v_med3_f32 v3, v3, s82, v229
	v_cvt_pk_fp8_f32 v1, v2, v3 op_sel:[0,0,1]
	v_or_b32_e32 v10, s8, v12
	s_nop 0
	v_lshlrev_b64 v[2:3], 10, v[10:11]
	v_lshl_add_u64 v[2:3], v[8:9], 0, v[2:3]
	global_store_dwordx2 v[2:3], v[0:1], off
	s_waitcnt lgkmcnt(0)
	s_barrier
	s_add_i32 s27, s27, 1
	s_cmp_lg_u32 s27, s24
	s_cbranch_scc0 .LBB0_806

.LBB0_721:
	s_mov_b32 s3, s97
	s_mov_b32 s28, s2
	s_waitcnt vmcnt(0)
	v_mbcnt_lo_u32_b32 v0, -1, s3
	s_ashr_i32 s3, s2, 31
	s_nop 0
	v_mbcnt_hi_u32_b32 v0, -1, v0
	s_lshl_b64 s[4:5], s[2:3], 14
	v_add_u32_e32 v0, s64, v0
	s_add_u32 s4, s90, s4
	s_addc_u32 s5, s91, s5
	v_ashrrev_i32_e32 v1, 31, v0
	s_nop 0
	v_lshl_add_u64 v[2:3], v[0:1], 2, s[4:5]
	v_add_co_u32_e32 v4, vcc, s75, v2
	s_nop 0
	global_load_dword v1, v[2:3], off
	global_load_dword v8, v[2:3], off offset:2048
	v_addc_co_u32_e32 v5, vcc, 0, v3, vcc
	v_add_co_u32_e32 v6, vcc, s66, v2
	v_lshl_add_u32 v0, v0, 2, 0
	s_nop 0
	v_addc_co_u32_e32 v7, vcc, 0, v3, vcc
	v_add_co_u32_e32 v2, vcc, 0x3000, v2
	global_load_dword v9, v[6:7], off offset:-4096
	s_nop 0
	s_nop 0
	global_load_dword v4, v[4:5], off offset:2048
	s_nop 0
	s_nop 0
	global_load_dword v5, v[6:7], off
	s_nop 0
	s_nop 0
	global_load_dword v6, v[6:7], off offset:2048
	v_addc_co_u32_e32 v3, vcc, 0, v3, vcc
	s_nop 0
	global_load_dword v7, v[2:3], off
	s_nop 0
	s_nop 0
	global_load_dword v2, v[2:3], off offset:2048
	v_add_u32_e32 v0, 0x15000, v0
	s_waitcnt vmcnt(6)
	s_nop 0
	ds_write2st64_b32 v0, v1, v8 offset1:8
	s_waitcnt vmcnt(4)
	s_nop 0
	ds_write2st64_b32 v0, v9, v4 offset0:16 offset1:24
	s_waitcnt vmcnt(2)
	s_nop 0
	ds_write2st64_b32 v0, v5, v6 offset0:32 offset1:40
	s_waitcnt vmcnt(0)
	s_nop 0
	ds_write2st64_b32 v0, v7, v2 offset0:48 offset1:56
	s_waitcnt vmcnt(0) lgkmcnt(0)
	s_barrier
.LBB0_722:
	s_ashr_i32 s3, s2, 31
	s_lshr_b32 s3, s3, 28
	s_add_i32 s3, s2, s3
	s_ashr_i32 s4, s3, 4
	s_and_b32 s3, s3, 0x3fffff0
	s_sub_i32 s10, s2, s3
	s_mov_b32 s2, s97
	s_ashr_i32 s5, s4, 31
	s_waitcnt vmcnt(0)
	v_mbcnt_lo_u32_b32 v0, -1, s2
	v_mbcnt_hi_u32_b32 v0, -1, v0
	v_add_u32_e32 v118, s64, v0
	s_lshl_b64 s[2:3], s[4:5], 12
	v_readfirstlane_b32 s41, v118
	s_ashr_i32 s29, s41, 6
	s_lshl_b32 s45, s40, 8
	s_add_u32 s2, s2, s45
	s_addc_u32 s3, s3, 0
	s_lshl_b32 s19, s29, 5
	s_ashr_i32 s9, s19, 31
	s_add_u32 s8, s2, s19
	s_addc_u32 s9, s3, s9
	s_lshl_b64 s[2:3], s[8:9], 11
	v_readlane_b32 s12, v254, 26
	v_readlane_b32 s13, v254, 27
	s_add_u32 s2, s12, s2
	s_addc_u32 s3, s13, s3
	s_lshl_b32 s10, s10, 6
	s_ashr_i32 s11, s10, 31
	s_lshl_b64 s[12:13], s[10:11], 1
	s_add_u32 s2, s2, s12
	s_addc_u32 s3, s3, s13
	s_lshl_b64 s[14:15], s[4:5], 23
	s_add_u32 s4, s54, s14
	s_addc_u32 s5, s55, s15
	s_add_u32 s4, s4, s12
	s_addc_u32 s5, s5, s13
	s_add_u32 s16, s25, s14
	v_and_b32_e32 v199, 63, v118
	s_addc_u32 s17, s26, s15
	s_add_u32 s16, s16, s12
	v_lshlrev_b32_e32 v96, 11, v199
	s_addc_u32 s17, s17, s13
	v_lshl_add_u64 v[0:1], s[4:5], 0, v[96:97]
	s_lshl_b32 s4, s29, 3
	s_ashr_i32 s5, s4, 31
	s_lshl_b32 s18, s29, 4
	s_nop 0
	v_bfe_u32 v241, v118, 2, 4
	v_lshl_add_u64 v[114:115], s[4:5], 1, v[0:1]
	v_and_or_b32 v0, s18, 48, v241
	v_lshlrev_b32_e32 v0, 11, v0
	v_mov_b32_e32 v1, v97
	v_lshl_add_u64 v[0:1], s[16:17], 0, v[0:1]
	s_ashr_i32 s16, s41, 3
	s_andn2_b32 s16, s16, 31
	s_ashr_i32 s17, s16, 31
	s_lshl_b32 s18, s29, 10
	v_lshlrev_b32_e32 v203, 3, v118
	s_cmp_lg_u32 0, -1
	v_and_b32_e32 v216, 24, v203
	s_cselect_b32 s20, 0, 0
	v_lshl_add_u64 v[0:1], s[16:17], 1, v[0:1]
	v_lshlrev_b32_e32 v2, 1, v216
	v_mov_b32_e32 v3, v97
	s_add_i32 s30, s18, s20
	s_mov_b32 s20, m0
	s_mov_b32 m0, s30
	s_nop 0
	global_load_lds_dwordx4 v[114:115], off
	s_mov_b32 m0, s20
	s_nop 0
	v_lshl_add_u64 v[116:117], v[0:1], 0, v[2:3]
	s_add_i32 s31, s30, 0x6000
	s_mov_b32 s20, m0
	s_mov_b32 m0, s31
	s_nop 0
	s_nop 0
	global_load_lds_dwordx4 v[116:117], off
	s_mov_b32 m0, s20
	s_nop 0
	v_bfe_u32 v215, v118, 5, 1
	s_mov_b64 s[20:21], 0x20000
	v_and_b32_e32 v214, 31, v118
	s_nop 0
	v_lshl_add_u64 v[0:1], v[114:115], 0, s[20:21]
	v_lshlrev_b32_e32 v2, 4, v215
	s_nop 0
	s_add_i32 s20, s30, 0x2000
	s_mov_b32 s21, m0
	s_mov_b32 m0, s20
	s_nop 0
	s_nop 0
	global_load_lds_dwordx4 v[0:1], off
	s_mov_b32 m0, s21
	s_nop 0
	v_lshl_or_b32 v0, v214, 11, v2
	global_load_dwordx4 v[110:113], v0, s[2:3]
	global_load_dwordx4 v[106:109], v0, s[2:3] offset:32
	global_load_dwordx4 v[102:105], v0, s[2:3] offset:64
	global_load_dwordx4 v[98:101], v0, s[2:3] offset:96
	v_lshl_add_u64 v[0:1], v[114:115], 0, s[62:63]
	s_add_i32 s2, s30, 0x4000
	s_mov_b32 s3, m0
	s_mov_b32 m0, s2
	s_nop 0
	s_nop 0
	global_load_lds_dwordx4 v[0:1], off
	s_mov_b32 m0, s3
	v_add_u32_e32 v0, 0, v2
	s_waitcnt vmcnt(3) lgkmcnt(0)
	s_barrier
	v_add_u32_e32 v12, 0x15000, v0
	ds_read_b128 v[16:19], v12
	ds_read_b128 v[0:3], v12 offset:128
	v_lshlrev_b32_e32 v236, 2, v215
	v_lshlrev_b32_e32 v32, 10, v215
	v_lshlrev_b32_e32 v33, 4, v214
	s_nop 0
	ds_read_b128 v[20:23], v12 offset:32
	ds_read_b128 v[4:7], v12 offset:160
	ds_read_b128 v[24:27], v12 offset:64
	ds_read_b128 v[8:11], v12 offset:192
	ds_read_b128 v[28:31], v12 offset:96
	ds_read_b128 v[12:15], v12 offset:224
	v_add3_u32 v238, 0, v32, v33
	ds_read_b128 v[32:35], v238
	s_cmp_lg_u32 s40, 0
	s_cselect_b64 s[2:3], -1, 0
	v_or_b32_e32 v237, s19, v214
	s_and_b64 vcc, exec, s[2:3]
	s_waitcnt vmcnt(3) lgkmcnt(0)
	s_nop 0
	v_mfma_f32_32x32x16_bf16 v[16:31], v[32:35], v[110:113], v[16:31]
	ds_read_b128 v[32:35], v238 offset:512
	s_waitcnt lgkmcnt(0)
	s_nop 0
	v_mfma_f32_32x32x16_bf16 v[0:15], v[32:35], v[110:113], v[0:15]
	ds_read_b128 v[32:35], v238 offset:2048
	s_waitcnt vmcnt(2) lgkmcnt(0)
	s_nop 0
	v_mfma_f32_32x32x16_bf16 v[16:31], v[32:35], v[106:109], v[16:31]
	ds_read_b128 v[32:35], v238 offset:2560
	s_waitcnt lgkmcnt(0)
	s_nop 0
	v_mfma_f32_32x32x16_bf16 v[0:15], v[32:35], v[106:109], v[0:15]
	ds_read_b128 v[32:35], v238 offset:4096
	s_waitcnt vmcnt(1) lgkmcnt(0)
	s_nop 0
	v_mfma_f32_32x32x16_bf16 v[16:31], v[32:35], v[102:105], v[16:31]
	ds_read_b128 v[32:35], v238 offset:4608
	s_waitcnt lgkmcnt(0)
	s_nop 0
	v_mfma_f32_32x32x16_bf16 v[0:15], v[32:35], v[102:105], v[0:15]
	ds_read_b128 v[32:35], v238 offset:6144
	s_waitcnt vmcnt(0) lgkmcnt(0)
	s_nop 0
	v_mfma_f32_32x32x16_bf16 v[16:31], v[32:35], v[98:101], v[16:31]
	ds_read_b128 v[32:35], v238 offset:6656
	s_waitcnt lgkmcnt(0)
	s_nop 0
	v_mfma_f32_32x32x16_bf16 v[0:15], v[32:35], v[98:101], v[0:15]
	s_nop 15
	s_nop 7
	s_cbranch_vccnz .LBB0_724
	v_or_b32_e32 v32, 32, v236
	v_cmp_le_i32_e32 vcc, v32, v237
	v_or_b32_e32 v32, 33, v236
	s_nop 7
	v_cndmask_b32_e32 v0, v232, v0, vcc
	v_cmp_lt_i32_e32 vcc, v236, v237
	s_nop 1
	v_cndmask_b32_e32 v17, v232, v17, vcc
	v_cmp_le_i32_e32 vcc, v236, v237
	s_nop 1
	v_cndmask_b32_e32 v16, v232, v16, vcc
	v_cmp_le_i32_e32 vcc, v32, v237
	v_or_b32_e32 v32, 2, v236
	s_nop 0
	v_cndmask_b32_e32 v1, v232, v1, vcc
	v_cmp_le_i32_e32 vcc, v32, v237
	v_or_b32_e32 v32, 34, v236
	s_nop 0
	v_cndmask_b32_e32 v18, v232, v18, vcc
	v_cmp_le_i32_e32 vcc, v32, v237
	v_or_b32_e32 v32, 3, v236
	s_nop 0
	v_cndmask_b32_e32 v2, v232, v2, vcc
	v_cmp_le_i32_e32 vcc, v32, v237
	v_or_b32_e32 v32, 35, v236
	s_nop 0
	v_cndmask_b32_e32 v19, v232, v19, vcc
	v_cmp_le_i32_e32 vcc, v32, v237
	v_or_b32_e32 v32, 8, v236
	s_nop 0
	v_cndmask_b32_e32 v3, v232, v3, vcc
	v_cmp_le_i32_e32 vcc, v32, v237
	v_or_b32_e32 v32, 40, v236
	s_nop 0
	v_cndmask_b32_e32 v20, v232, v20, vcc
	v_cmp_le_i32_e32 vcc, v32, v237
	v_or_b32_e32 v32, 9, v236
	s_nop 0
	v_cndmask_b32_e32 v4, v232, v4, vcc
	v_cmp_le_i32_e32 vcc, v32, v237
	v_or_b32_e32 v32, 41, v236
	s_nop 0
	v_cndmask_b32_e32 v21, v232, v21, vcc
	v_cmp_le_i32_e32 vcc, v32, v237
	v_or_b32_e32 v32, 10, v236
	s_nop 0
	v_cndmask_b32_e32 v5, v232, v5, vcc
	v_cmp_le_i32_e32 vcc, v32, v237
	v_or_b32_e32 v32, 42, v236
	s_nop 0
	v_cndmask_b32_e32 v22, v232, v22, vcc
	v_cmp_le_i32_e32 vcc, v32, v237
	v_or_b32_e32 v32, 11, v236
	s_nop 0
	v_cndmask_b32_e32 v6, v232, v6, vcc
	v_cmp_le_i32_e32 vcc, v32, v237
	v_or_b32_e32 v32, 43, v236
	s_nop 0
	v_cndmask_b32_e32 v23, v232, v23, vcc
	v_cmp_le_i32_e32 vcc, v32, v237
	v_or_b32_e32 v32, 16, v236
	s_nop 0
	v_cndmask_b32_e32 v7, v232, v7, vcc
	v_cmp_le_i32_e32 vcc, v32, v237
	v_or_b32_e32 v32, 48, v236
	s_nop 0
	v_cndmask_b32_e32 v24, v232, v24, vcc
	v_cmp_le_i32_e32 vcc, v32, v237
	v_or_b32_e32 v32, 17, v236
	s_nop 0
	v_cndmask_b32_e32 v8, v232, v8, vcc
	v_cmp_le_i32_e32 vcc, v32, v237
	v_or_b32_e32 v32, 49, v236
	s_nop 0
	v_cndmask_b32_e32 v25, v232, v25, vcc
	v_cmp_le_i32_e32 vcc, v32, v237
	v_or_b32_e32 v32, 18, v236
	s_nop 0
	v_cndmask_b32_e32 v9, v232, v9, vcc
	v_cmp_le_i32_e32 vcc, v32, v237
	v_or_b32_e32 v32, 50, v236
	s_nop 0
	v_cndmask_b32_e32 v26, v232, v26, vcc
	v_cmp_le_i32_e32 vcc, v32, v237
	v_or_b32_e32 v32, 19, v236
	s_nop 0
	v_cndmask_b32_e32 v10, v232, v10, vcc
	v_cmp_le_i32_e32 vcc, v32, v237
	v_or_b32_e32 v32, 51, v236
	s_nop 0
	v_cndmask_b32_e32 v27, v232, v27, vcc
	v_cmp_le_i32_e32 vcc, v32, v237
	v_or_b32_e32 v32, 24, v236
	s_nop 0
	v_cndmask_b32_e32 v11, v232, v11, vcc
	v_cmp_le_i32_e32 vcc, v32, v237
	v_or_b32_e32 v32, 56, v236
	s_nop 0
	v_cndmask_b32_e32 v28, v232, v28, vcc
	v_cmp_le_i32_e32 vcc, v32, v237
	v_or_b32_e32 v32, 25, v236
	s_nop 0
	v_cndmask_b32_e32 v12, v232, v12, vcc
	v_cmp_le_i32_e32 vcc, v32, v237
	v_or_b32_e32 v32, 57, v236
	s_nop 0
	v_cndmask_b32_e32 v29, v232, v29, vcc
	v_cmp_le_i32_e32 vcc, v32, v237
	v_or_b32_e32 v32, 26, v236
	s_nop 0
	v_cndmask_b32_e32 v13, v232, v13, vcc
	v_cmp_le_i32_e32 vcc, v32, v237
	v_or_b32_e32 v32, 58, v236
	s_nop 0
	v_cndmask_b32_e32 v30, v232, v30, vcc
	v_cmp_le_i32_e32 vcc, v32, v237
	v_or_b32_e32 v32, 27, v236
	s_nop 0
	v_cndmask_b32_e32 v14, v232, v14, vcc
	v_cmp_le_i32_e32 vcc, v32, v237
	v_or_b32_e32 v32, 59, v236
	s_nop 0
	v_cndmask_b32_e32 v31, v232, v31, vcc
	v_cmp_le_i32_e32 vcc, v32, v237
	s_nop 1
	v_cndmask_b32_e32 v15, v232, v15, vcc
.LBB0_724:
	v_lshlrev_b32_e32 v32, 1, v118
	v_and_b32_e32 v218, 32, v32
	v_lshrrev_b32_e32 v32, 2, v118
	v_and_or_b32 v32, v32, 3, v236
	v_lshlrev_b32_e32 v217, 6, v32
	v_add_u32_e32 v32, 0, v218
	v_add3_u32 v239, v32, v216, v217
	v_max3_f32 v32, v16, v17, v0
	v_max3_f32 v33, v18, v19, v1
	s_and_b32 s19, s41, 0x3fffffc0
	v_max3_f32 v32, v32, v2, v3
	v_max3_f32 v33, v33, v22, v23
	s_add_i32 s20, s45, 0x100
	v_max3_f32 v32, v32, v20, v21
	v_max3_f32 v33, v33, v6, v7
	s_lshl_b32 s19, s19, 2
	s_nop 0
	v_max3_f32 v32, v32, v4, v5
	v_max3_f32 v33, v33, v26, v27
	s_lshr_b32 s39, s20, 6
	s_nop 0
	v_max3_f32 v32, v32, v24, v25
	v_max3_f32 v33, v33, v10, v11
	s_mov_b64 s[20:21], 0x60000
	v_max3_f32 v32, v32, v8, v9
	v_max3_f32 v33, v33, v30, v31
	s_add_i32 s19, s19, 0
	s_nop 0
	v_max3_f32 v32, v32, v28, v29
	v_max3_f32 v33, v33, v14, v15
	s_cmp_lg_u32 0, -1
	s_nop 0
	v_max3_f32 v32, v32, v12, v13
	s_mov_b32 s96, 1
	v_max_f32_e32 v32, v32, v33
	s_mov_b32 s22, 0
	v_mov_b32_e32 v33, v32
	s_nop 1
	v_permlane32_swap_b32_e32 v32, v33
	v_max_f32_e64 v32, v32, v33
	v_lshl_add_u32 v235, v214, 2, s19
	v_sub_f32_e32 v64, v0, v32
	v_sub_f32_e32 v0, v17, v32
	v_sub_f32_e32 v16, v16, v32
	v_sub_f32_e32 v65, v1, v32
	v_sub_f32_e32 v1, v18, v32
	v_sub_f32_e32 v66, v2, v32
	v_sub_f32_e32 v2, v19, v32
	s_nop 0
	v_exp_f32_e64 v81, v0
	v_lshl_add_u32 v0, v236, 2, 0
	v_sub_f32_e32 v67, v3, v32
	v_sub_f32_e32 v3, v20, v32
	v_sub_f32_e32 v68, v4, v32
	v_sub_f32_e32 v4, v21, v32
	v_sub_f32_e32 v69, v5, v32
	v_sub_f32_e32 v5, v22, v32
	v_sub_f32_e32 v70, v6, v32
	v_sub_f32_e32 v6, v23, v32
	v_sub_f32_e32 v71, v7, v32
	v_sub_f32_e32 v7, v24, v32
	v_sub_f32_e32 v72, v8, v32
	v_sub_f32_e32 v8, v25, v32
	v_sub_f32_e32 v73, v9, v32
	v_sub_f32_e32 v9, v26, v32
	v_sub_f32_e32 v74, v10, v32
	v_sub_f32_e32 v10, v27, v32
	v_sub_f32_e32 v75, v11, v32
	v_sub_f32_e32 v11, v28, v32
	v_sub_f32_e32 v76, v12, v32
	v_sub_f32_e32 v12, v29, v32
	v_sub_f32_e32 v77, v13, v32
	v_sub_f32_e32 v13, v30, v32
	v_sub_f32_e32 v78, v14, v32
	v_sub_f32_e32 v14, v31, v32
	v_add_u32_e32 v28, 0x15100, v0
	v_sub_f32_e32 v79, v15, v32
	v_exp_f32_e32 v80, v16
	v_exp_f32_e32 v82, v1
	v_exp_f32_e32 v83, v2
	v_exp_f32_e32 v84, v3
	v_exp_f32_e32 v85, v4
	v_exp_f32_e32 v86, v5
	v_exp_f32_e32 v87, v6
	v_exp_f32_e32 v88, v7
	v_exp_f32_e32 v89, v8
	v_exp_f32_e32 v90, v9
	v_exp_f32_e32 v91, v10
	v_exp_f32_e32 v92, v11
	v_exp_f32_e32 v93, v12
	v_exp_f32_e32 v94, v13
	v_exp_f32_e32 v95, v14
	ds_read_b128 v[0:3], v28
	ds_read_b128 v[4:7], v28 offset:32
	ds_read_b128 v[8:11], v28 offset:128
	ds_read_b128 v[12:15], v28 offset:160
	ds_read_b128 v[16:19], v28 offset:64
	ds_read_b128 v[20:23], v28 offset:96
	ds_read_b128 v[24:27], v28 offset:192
	ds_read_b128 v[28:31], v28 offset:224
	s_waitcnt vmcnt(0) lgkmcnt(0)
	s_barrier
	v_add_f32_e64 v202, v97, v32
	v_exp_f32_e32 v64, v64
	s_waitcnt lgkmcnt(7)
	v_pk_add_f32 v[48:49], v[202:203], v[0:1] op_sel_hi:[0,1] neg_lo:[1,0] neg_hi:[1,0]
	v_lshl_add_u64 v[0:1], v[114:115], 0, s[20:21]
	s_mov_b32 s20, m0
	s_mov_b32 m0, s30
	s_nop 0
	s_nop 0
	global_load_lds_dwordx4 v[0:1], off
	s_mov_b32 m0, s20
	s_nop 0
	s_mov_b64 s[20:21], 0x20000
	v_lshl_add_u64 v[0:1], v[116:117], 0, s[20:21]
	s_cselect_b32 s20, 0, 0
	s_add_i32 s18, s20, s18
	s_add_i32 s18, s18, 0x8000
	s_mov_b32 s20, m0
	s_mov_b32 m0, s18
	s_nop 0
	s_nop 0
	global_load_lds_dwordx4 v[0:1], off
	s_mov_b32 m0, s20
	s_nop 0
	ds_read_b128 v[158:161], v238 offset:8192
	ds_read_b128 v[146:149], v238 offset:8704
	ds_read_b128 v[154:157], v238 offset:10240
	ds_read_b128 v[142:145], v238 offset:10752
	ds_read_b128 v[150:153], v238 offset:12288
	ds_read_b128 v[138:141], v238 offset:12800
	ds_read_b128 v[134:137], v238 offset:14336
	ds_read_b128 v[130:133], v238 offset:14848
	v_exp_f32_e32 v65, v65
	v_exp_f32_e32 v66, v66
	v_exp_f32_e32 v67, v67
	v_exp_f32_e32 v68, v68
	v_exp_f32_e32 v69, v69
	v_exp_f32_e32 v70, v70
	v_exp_f32_e32 v71, v71
	v_exp_f32_e32 v72, v72
	v_exp_f32_e32 v73, v73
	v_exp_f32_e32 v74, v74
	v_exp_f32_e32 v75, v75
	v_exp_f32_e32 v76, v76
	v_exp_f32_e32 v77, v77
	v_exp_f32_e32 v78, v78
	v_exp_f32_e64 v79, v79
	s_waitcnt vmcnt(2) lgkmcnt(0)
	s_barrier
	v_and_b32_e32 v0, 3, v118
	s_waitcnt lgkmcnt(13)
	v_pk_add_f32 v[32:33], v[202:203], v[8:9] op_sel_hi:[0,1] neg_lo:[1,0] neg_hi:[1,0]
	v_pk_add_f32 v[50:51], v[202:203], v[2:3] op_sel_hi:[0,1] neg_lo:[1,0] neg_hi:[1,0]
	v_pk_add_f32 v[34:35], v[202:203], v[10:11] op_sel_hi:[0,1] neg_lo:[1,0] neg_hi:[1,0]
	v_pk_add_f32 v[52:53], v[202:203], v[4:5] op_sel_hi:[0,1] neg_lo:[1,0] neg_hi:[1,0]
	s_waitcnt lgkmcnt(12)
	s_nop 0
	v_pk_add_f32 v[36:37], v[202:203], v[12:13] op_sel_hi:[0,1] neg_lo:[1,0] neg_hi:[1,0]
	v_pk_add_f32 v[54:55], v[202:203], v[6:7] op_sel_hi:[0,1] neg_lo:[1,0] neg_hi:[1,0]
	v_pk_add_f32 v[38:39], v[202:203], v[14:15] op_sel_hi:[0,1] neg_lo:[1,0] neg_hi:[1,0]
	s_waitcnt lgkmcnt(11)
	s_nop 0
	v_pk_add_f32 v[56:57], v[202:203], v[16:17] op_sel_hi:[0,1] neg_lo:[1,0] neg_hi:[1,0]
	s_waitcnt lgkmcnt(9)
	s_nop 0
	v_pk_add_f32 v[40:41], v[202:203], v[24:25] op_sel_hi:[0,1] neg_lo:[1,0] neg_hi:[1,0]
	v_pk_add_f32 v[58:59], v[202:203], v[18:19] op_sel_hi:[0,1] neg_lo:[1,0] neg_hi:[1,0]
	v_pk_add_f32 v[42:43], v[202:203], v[26:27] op_sel_hi:[0,1] neg_lo:[1,0] neg_hi:[1,0]
	v_pk_add_f32 v[60:61], v[202:203], v[20:21] op_sel_hi:[0,1] neg_lo:[1,0] neg_hi:[1,0]
	s_waitcnt lgkmcnt(8)
	s_nop 0
	v_pk_add_f32 v[44:45], v[202:203], v[28:29] op_sel_hi:[0,1] neg_lo:[1,0] neg_hi:[1,0]
	v_pk_add_f32 v[62:63], v[202:203], v[22:23] op_sel_hi:[0,1] neg_lo:[1,0] neg_hi:[1,0]
	v_pk_add_f32 v[46:47], v[202:203], v[30:31] op_sel_hi:[0,1] neg_lo:[1,0] neg_hi:[1,0]
	s_andn2_b64 vcc, exec, s[2:3]
	s_nop 0
	v_cmp_gt_u32_e64 s[2:3], 32, v199
	v_lshl_add_u32 v219, v236, 2, s19
	v_lshlrev_b32_e32 v204, 4, v0
	s_cbranch_vccnz .LBB0_742
	s_lshl_b64 s[18:19], s[4:5], 1
	s_add_u32 s18, s70, s18
	s_addc_u32 s19, s71, s19
	s_add_u32 s18, s18, s14
	s_addc_u32 s19, s19, s15
	s_nop 0
	v_lshl_add_u64 v[206:207], s[18:19], 0, v[96:97]
	s_lshl_b64 s[18:19], s[16:17], 1
	s_add_u32 s18, s18, s14
	v_mov_b32_e32 v205, v97
	s_addc_u32 s19, s19, s15
	v_lshl_add_u64 v[0:1], s[18:19], 0, v[204:205]
	s_lshl_b32 s18, s41, 9
	s_nop 0
	s_and_b32 s18, s18, 0x18000
	v_lshl_or_b32 v2, v241, 11, s18
	v_mov_b32_e64 v3, v97
	v_lshl_add_u64 v[0:1], v[0:1], 0, v[2:3]
	v_mov_b32_e32 v16, v97
	v_mov_b32_e32 v17, v97
	v_lshl_add_u64 v[208:209], s[70:71], 0, v[0:1]
	v_subrev_u32_e64 v245, s14, v0
	v_add_u32_e32 v245, 0x7fc0000, v245
	v_lshl_add_u32 v244, s4, 1, v96
	s_add_u32 s98, s70, s14
	s_addc_u32 s99, s71, s15
	s_add_u32 s98, s98, s12
	s_addc_u32 s99, s99, s13
	s_add_u32 s98, s98, 0x16e80000
	s_addc_u32 s99, s99, 0
	s_nop 0
	v_readlane_b32 s18, v253, 11
	v_mov_b32_e32 v18, v97
	v_mov_b32_e32 v19, v97
	v_mov_b32_e32 v20, v97
	v_mov_b32_e32 v21, v97
	v_mov_b32_e32 v22, v97
	v_mov_b32_e32 v23, v97
	v_mov_b32_e32 v24, v97
	v_mov_b32_e32 v25, v97
	v_mov_b32_e32 v26, v97
	v_mov_b32_e32 v27, v97
	v_mov_b32_e32 v28, v97
	v_mov_b32_e32 v29, v97
	v_mov_b32_e64 v30, v97
	v_mov_b32_e32 v31, v97
	v_mov_b64_e32 v[0:1], v[16:17]
	v_lshl_add_u32 v205, v215, 4, s18
	s_mov_b32 s18, 0
	s_movk_i32 s22, 0x4000
	s_movk_i32 s38, 0x2000
	v_mov_b32_e32 v240, 0
	s_mov_b32 s23, 6
	v_mov_b64_e32 v[2:3], v[18:19]
	v_mov_b64_e32 v[4:5], v[20:21]
	v_mov_b64_e32 v[6:7], v[22:23]
	v_mov_b64_e32 v[8:9], v[24:25]
	v_mov_b64_e32 v[10:11], v[26:27]
	v_mov_b64_e32 v[12:13], v[28:29]
	v_mov_b64_e32 v[14:15], v[30:31]

.LBB0_737:
	v_max_f32_e32 v48, v48, v48
	v_max_f32_e32 v49, 0, v48
	v_exp_f32_e64 v48, -v49
	s_and_saveexec_b64 s[20:21], s[2:3]
	s_nop 0
	ds_write_b32 v235, v48 offset:49152
	s_or_b64 exec, exec, s[20:21]
	v_sub_f32_e32 v95, v95, v49
	v_sub_f32_e32 v94, v94, v49
	v_sub_f32_e32 v93, v93, v49
	v_sub_f32_e32 v92, v92, v49
	v_sub_f32_e32 v91, v91, v49
	v_sub_f32_e32 v90, v90, v49
	v_sub_f32_e32 v89, v89, v49
	v_sub_f32_e32 v88, v88, v49
	v_sub_f32_e32 v87, v87, v49
	v_sub_f32_e32 v86, v86, v49
	v_sub_f32_e32 v85, v85, v49
	v_sub_f32_e32 v84, v84, v49
	v_sub_f32_e32 v83, v83, v49
	v_sub_f32_e32 v82, v82, v49
	v_sub_f32_e32 v81, v81, v49
	v_sub_f32_e32 v80, v80, v49
	v_sub_f32_e32 v79, v79, v49
	v_sub_f32_e32 v78, v78, v49
	v_sub_f32_e32 v77, v77, v49
	v_sub_f32_e32 v76, v76, v49
	v_sub_f32_e32 v75, v75, v49
	v_sub_f32_e32 v74, v74, v49
	v_sub_f32_e32 v73, v73, v49
	v_sub_f32_e32 v72, v72, v49
	v_sub_f32_e32 v71, v71, v49
	v_sub_f32_e32 v70, v70, v49
	v_sub_f32_e32 v69, v69, v49
	v_sub_f32_e32 v68, v68, v49
	v_sub_f32_e32 v67, v67, v49
	v_sub_f32_e32 v66, v66, v49
	v_sub_f32_e32 v65, v65, v49
	v_sub_f32_e32 v64, v64, v49
	v_add_f32_e32 v202, v202, v49
	v_mul_f32_e64 v240, v240, v48
	s_branch .LBB0_730

.LBB0_744:
	v_add_u32_e32 v96, s46, v239
	ds_read_b64_tr_b16 v[162:163], v96 offset:24576
	ds_read_b64_tr_b16 v[164:165], v96 offset:25088
	s_waitcnt lgkmcnt(9)
	s_nop 0
	v_mfma_f32_32x32x16_bf16 v[48:63], v[158:161], v[110:113], v[48:63]
	v_add_f32_e32 v114, v80, v81
	v_add_f32_e32 v114, v82, v114
	v_add_f32_e32 v114, v83, v114
	v_add_f32_e32 v114, v84, v114
	v_add_f32_e64 v114, v85, v114
	v_cvt_pk_bf16_f32 v126, v80, v81
	v_cvt_pk_bf16_f32 v127, v82, v83
	ds_read_b64_tr_b16 v[80:81], v96 offset:28672
	ds_read_b64_tr_b16 v[82:83], v96 offset:29184
	s_waitcnt lgkmcnt(10)
	s_nop 0
	v_mfma_f32_32x32x16_bf16 v[32:47], v[146:149], v[110:113], v[32:47]
	v_add_f32_e32 v110, v86, v114
	v_add_f32_e32 v110, v87, v110
	v_add_f32_e32 v110, v88, v110
	v_add_f32_e32 v110, v89, v110
	v_cvt_pk_bf16_f32 v128, v84, v85
	v_cvt_pk_bf16_f32 v129, v86, v87
	ds_read_b64_tr_b16 v[84:85], v96 offset:25600
	ds_read_b64_tr_b16 v[86:87], v96 offset:26112
	s_waitcnt lgkmcnt(11)
	s_nop 0
	v_mfma_f32_32x32x16_bf16 v[48:63], v[154:157], v[106:109], v[48:63]
	v_add_f32_e32 v110, v90, v110
	v_add_f32_e32 v110, v91, v110
	v_add_f32_e32 v110, v92, v110
	v_add_f32_e32 v110, v93, v110
	v_cvt_pk_bf16_f32 v122, v88, v89
	v_cvt_pk_bf16_f32 v123, v90, v91
	ds_read_b64_tr_b16 v[88:89], v96 offset:29696
	ds_read_b64_tr_b16 v[90:91], v96 offset:30208
	s_waitcnt lgkmcnt(12)
	s_nop 0
	v_mfma_f32_32x32x16_bf16 v[32:47], v[142:145], v[106:109], v[32:47]
	v_add_f32_e32 v106, v94, v110
	v_add_f32_e32 v106, v95, v106
	v_add_f32_e32 v106, v64, v106
	v_add_f32_e32 v106, v65, v106
	v_cvt_pk_bf16_f32 v124, v92, v93
	v_cvt_pk_bf16_f32 v125, v94, v95
	ds_read_b64_tr_b16 v[92:93], v96 offset:26624
	ds_read_b64_tr_b16 v[94:95], v96 offset:27136
	s_waitcnt lgkmcnt(13)
	s_nop 0
	v_mfma_f32_32x32x16_bf16 v[48:63], v[150:153], v[102:105], v[48:63]
	v_add_f32_e32 v106, v66, v106
	v_add_f32_e32 v106, v67, v106
	v_add_f32_e32 v106, v68, v106
	v_add_f32_e32 v106, v69, v106
	v_cvt_pk_bf16_f32 v118, v64, v65
	v_cvt_pk_bf16_f32 v119, v66, v67
	ds_read_b64_tr_b16 v[64:65], v96 offset:30720
	ds_read_b64_tr_b16 v[66:67], v96 offset:31232
	s_waitcnt lgkmcnt(14)
	s_nop 0
	v_mfma_f32_32x32x16_bf16 v[32:47], v[138:141], v[102:105], v[32:47]
	v_add_f32_e32 v102, v70, v106
	v_add_f32_e32 v102, v71, v102
	v_add_f32_e32 v102, v72, v102
	v_add_f32_e32 v102, v73, v102
	v_cvt_pk_bf16_f32 v120, v68, v69
	v_cvt_pk_bf16_f32 v121, v70, v71
	ds_read_b64_tr_b16 v[68:69], v96 offset:27648
	ds_read_b64_tr_b16 v[70:71], v96 offset:28160
	s_waitcnt lgkmcnt(14)
	s_nop 0
	v_mfma_f32_32x32x16_bf16 v[48:63], v[134:137], v[98:101], v[48:63]
	v_add_f32_e32 v102, v74, v102
	v_add_f32_e32 v102, v75, v102
	v_add_f32_e32 v102, v76, v102
	v_add_f32_e32 v102, v77, v102
	v_cvt_pk_bf16_f32 v114, v72, v73
	v_cvt_pk_bf16_f32 v115, v74, v75
	ds_read_b64_tr_b16 v[72:73], v96 offset:31744
	ds_read_b64_tr_b16 v[74:75], v96 offset:32256
	v_mfma_f32_32x32x16_bf16 v[32:47], v[130:133], v[98:101], v[32:47]
	v_add_f32_e32 v96, v78, v102
	v_add_f32_e32 v96, v79, v96
	v_add_f32_e64 v96, 0, v96
	v_cvt_pk_bf16_f32 v116, v76, v77
	v_cvt_pk_bf16_f32 v117, v78, v79
	v_or_b32_e32 v77, 0xe0, v236
	v_or_b32_e32 v76, 0xc0, v236
	v_cmp_le_i32_e32 vcc, v77, v237
	s_nop 3
	v_cndmask_b32_e32 v32, v232, v32, vcc
	v_cmp_lt_i32_e32 vcc, v76, v237
	s_nop 1
	v_cndmask_b32_e32 v49, v232, v49, vcc
	v_cmp_le_i32_e32 vcc, v76, v237
	s_nop 0
	v_or_b32_e32 v76, 0xe1, v236
	s_nop 0
	v_cndmask_b32_e32 v48, v232, v48, vcc
	v_cmp_le_i32_e32 vcc, v76, v237
	s_nop 0
	v_or_b32_e32 v76, 0xc2, v236
	v_max_f32_e64 v77, v48, v48
	v_cndmask_b32_e32 v33, v232, v33, vcc
	v_cmp_le_i32_e32 vcc, v76, v237
	v_or_b32_e32 v76, 0xe2, v236
	s_nop 0
	v_cndmask_b32_e32 v50, v232, v50, vcc
	v_cmp_le_i32_e32 vcc, v76, v237
	s_nop 0
	v_or_b32_e32 v76, 0xc3, v236
	s_nop 0
	v_cndmask_b32_e32 v34, v232, v34, vcc
	v_cmp_le_i32_e32 vcc, v76, v237
	s_nop 0
	v_or_b32_e32 v76, 0xe3, v236
	s_nop 0
	v_cndmask_b32_e32 v51, v232, v51, vcc
	v_cmp_le_i32_e32 vcc, v76, v237
	s_nop 0
	v_or_b32_e32 v76, 0xc8, v236
	s_nop 0
	v_cndmask_b32_e32 v35, v232, v35, vcc
	v_cmp_le_i32_e32 vcc, v76, v237
	s_nop 0
	v_or_b32_e32 v76, 0xe8, v236
	s_nop 0
	v_cndmask_b32_e32 v52, v232, v52, vcc
	v_cmp_le_i32_e32 vcc, v76, v237
	s_nop 0
	v_or_b32_e32 v76, 0xc9, v236
	s_nop 0
	v_cndmask_b32_e32 v36, v232, v36, vcc
	v_cmp_le_i32_e32 vcc, v76, v237
	s_nop 0
	v_or_b32_e32 v76, 0xe9, v236
	s_nop 0
	v_cndmask_b32_e32 v53, v232, v53, vcc
	v_cmp_le_i32_e32 vcc, v76, v237
	s_nop 0
	v_or_b32_e32 v76, 0xca, v236
	s_nop 0
	v_cndmask_b32_e32 v37, v232, v37, vcc
	v_cmp_le_i32_e32 vcc, v76, v237
	s_nop 0
	v_or_b32_e32 v76, 0xea, v236
	s_nop 0
	v_cndmask_b32_e32 v54, v232, v54, vcc
	v_cmp_le_i32_e32 vcc, v76, v237
	s_nop 0
	v_or_b32_e32 v76, 0xcb, v236
	s_nop 0
	v_cndmask_b32_e32 v38, v232, v38, vcc
	v_cmp_le_i32_e32 vcc, v76, v237
	s_nop 0
	v_or_b32_e32 v76, 0xeb, v236
	s_nop 0
	v_cndmask_b32_e32 v55, v232, v55, vcc
	v_cmp_le_i32_e32 vcc, v76, v237
	s_nop 0
	v_or_b32_e32 v76, 0xd0, v236
	s_nop 0
	v_cndmask_b32_e32 v39, v232, v39, vcc
	v_cmp_le_i32_e32 vcc, v76, v237
	s_nop 0
	v_or_b32_e32 v76, 0xf0, v236
	s_nop 0
	v_cndmask_b32_e32 v56, v232, v56, vcc
	v_cmp_le_i32_e32 vcc, v76, v237
	s_nop 0
	v_or_b32_e32 v76, 0xd1, v236
	s_nop 0
	v_cndmask_b32_e32 v40, v232, v40, vcc
	v_cmp_le_i32_e32 vcc, v76, v237
	s_nop 0
	v_or_b32_e32 v76, 0xf1, v236
	s_nop 0
	v_cndmask_b32_e32 v57, v232, v57, vcc
	v_cmp_le_i32_e32 vcc, v76, v237
	s_nop 0
	v_or_b32_e32 v76, 0xd2, v236
	s_nop 0
	v_cndmask_b32_e32 v41, v232, v41, vcc
	v_cmp_le_i32_e32 vcc, v76, v237
	s_nop 0
	v_or_b32_e32 v76, 0xf2, v236
	s_nop 0
	v_cndmask_b32_e32 v58, v232, v58, vcc
	v_cmp_le_i32_e32 vcc, v76, v237
	s_nop 0
	v_or_b32_e32 v76, 0xd3, v236
	s_nop 0
	v_cndmask_b32_e32 v42, v232, v42, vcc
	v_cmp_le_i32_e32 vcc, v76, v237
	s_nop 0
	v_or_b32_e32 v76, 0xf3, v236
	s_nop 0
	v_cndmask_b32_e32 v59, v232, v59, vcc
	v_cmp_le_i32_e32 vcc, v76, v237
	s_nop 0
	v_or_b32_e32 v76, 0xd8, v236
	s_nop 0
	v_cndmask_b32_e32 v43, v232, v43, vcc
	v_cmp_le_i32_e32 vcc, v76, v237
	s_nop 0
	v_or_b32_e32 v76, 0xf8, v236
	s_nop 0
	v_cndmask_b32_e32 v60, v232, v60, vcc
	v_cmp_le_i32_e32 vcc, v76, v237
	s_nop 0
	v_or_b32_e32 v76, 0xd9, v236
	s_nop 0
	v_cndmask_b32_e32 v44, v232, v44, vcc
	v_cmp_le_i32_e32 vcc, v76, v237
	s_nop 0
	v_or_b32_e32 v76, 0xf9, v236
	s_nop 0
	v_cndmask_b32_e32 v61, v232, v61, vcc
	v_cmp_le_i32_e32 vcc, v76, v237
	s_nop 0
	v_or_b32_e32 v76, 0xda, v236
	s_nop 0
	v_cndmask_b32_e32 v45, v232, v45, vcc
	v_cmp_le_i32_e32 vcc, v76, v237
	s_nop 0
	v_or_b32_e32 v76, 0xfa, v236
	s_nop 0
	v_cndmask_b32_e32 v62, v232, v62, vcc
	v_cmp_le_i32_e32 vcc, v76, v237
	s_nop 0
	v_or_b32_e32 v76, 0xdb, v236
	s_nop 0
	v_cndmask_b32_e32 v46, v232, v46, vcc
	v_cmp_le_i32_e32 vcc, v76, v237
	s_nop 0
	v_or_b32_e32 v76, 0xfb, v236
	s_nop 0
	v_cndmask_b32_e32 v63, v232, v63, vcc
	v_cmp_le_i32_e32 vcc, v76, v237
	v_max_f32_e32 v76, v49, v49
	v_max_f32_e64 v76, v77, v76
	v_max3_f32 v77, v50, v51, v33
	v_max3_f32 v76, v76, v32, v34
	v_max3_f32 v76, v76, v35, v52
	v_max3_f32 v77, v77, v54, v55
	v_max3_f32 v76, v76, v53, v36
	v_max3_f32 v77, v77, v38, v39
	v_max3_f32 v76, v76, v37, v56
	v_max3_f32 v77, v77, v58, v59
	v_max3_f32 v76, v76, v57, v40
	v_max3_f32 v77, v77, v42, v43
	v_cndmask_b32_e32 v47, v232, v47, vcc
	s_nop 0
	v_max3_f32 v76, v76, v41, v60
	v_max3_f32 v77, v77, v62, v63
	v_max3_f32 v78, v76, v61, v44
	v_max3_f32 v77, v77, v46, v47
	v_max3_f32 v77, v78, v45, v77
	v_mov_b32_e32 v78, v77
	s_nop 1
	v_permlane32_swap_b32_e32 v77, v78
	v_max_f32_e32 v78, v78, v78
	v_max_f32_e32 v77, v77, v77
	v_max_f32_e32 v77, v77, v78
	v_cmp_lt_f32_e32 vcc, s51, v77
	s_cmp_lg_u64 vcc, 0
	v_add_f32_e32 v76, v240, v96
	s_cselect_b64 s[2:3], -1, 0
	s_cbranch_vccnz .LBB0_803
.LBB0_745:
	s_waitcnt lgkmcnt(14)
	v_mfma_f32_32x32x16_bf16 v[16:31], v[126:129], v[162:165], v[16:31]
	v_exp_f32_e32 v48, v48
	v_exp_f32_e32 v49, v49
	v_exp_f32_e64 v50, v50
	v_exp_f32_e32 v51, v51
	s_waitcnt lgkmcnt(12)
	v_mfma_f32_32x32x16_bf16 v[0:15], v[126:129], v[80:83], v[0:15]
	v_exp_f32_e32 v52, v52
	v_exp_f32_e32 v53, v53
	v_exp_f32_e64 v54, v54
	v_exp_f32_e32 v55, v55
	s_waitcnt lgkmcnt(10)
	v_mfma_f32_32x32x16_bf16 v[16:31], v[122:125], v[84:87], v[16:31]
	v_exp_f32_e32 v56, v56
	v_exp_f32_e32 v57, v57
	v_exp_f32_e64 v58, v58
	v_exp_f32_e32 v59, v59
	s_waitcnt lgkmcnt(8)
	v_mfma_f32_32x32x16_bf16 v[0:15], v[122:125], v[88:91], v[0:15]
	v_exp_f32_e32 v60, v60
	v_exp_f32_e32 v61, v61
	v_exp_f32_e64 v62, v62
	v_exp_f32_e32 v63, v63
	s_waitcnt lgkmcnt(6)
	v_mfma_f32_32x32x16_bf16 v[16:31], v[118:121], v[92:95], v[16:31]
	v_exp_f32_e32 v32, v32
	v_exp_f32_e32 v33, v33
	v_exp_f32_e64 v34, v34
	v_exp_f32_e32 v35, v35
	s_waitcnt lgkmcnt(4)
	v_mfma_f32_32x32x16_bf16 v[0:15], v[118:121], v[64:67], v[0:15]
	v_exp_f32_e32 v36, v36
	v_exp_f32_e32 v37, v37
	v_exp_f32_e64 v38, v38
	v_exp_f32_e32 v39, v39
	s_waitcnt lgkmcnt(2)
	v_mfma_f32_32x32x16_bf16 v[16:31], v[114:117], v[68:71], v[16:31]
	v_exp_f32_e32 v40, v40
	v_exp_f32_e32 v41, v41
	v_exp_f32_e64 v42, v42
	v_exp_f32_e32 v43, v43
	s_waitcnt lgkmcnt(0)
	v_mfma_f32_32x32x16_bf16 v[0:15], v[114:117], v[72:75], v[0:15]
	v_exp_f32_e32 v44, v44
	v_exp_f32_e32 v45, v45
	v_exp_f32_e64 v46, v46
	v_exp_f32_e32 v47, v47
	s_andn2_b64 vcc, exec, s[2:3]
	s_cbranch_vccnz .LBB0_747
	s_waitcnt lgkmcnt(0)
	ds_read_b128 v[64:67], v219 offset:49248
	ds_read_b128 v[68:71], v219 offset:49216
	ds_read_b128 v[72:75], v219 offset:49184
	ds_read_b128 v[78:81], v219 offset:49152
	s_waitcnt lgkmcnt(3)
	s_nop 0
	v_pk_mul_f32 v[30:31], v[30:31], v[66:67]
	s_waitcnt lgkmcnt(2)
	s_nop 0
	v_pk_mul_f32 v[26:27], v[26:27], v[70:71]
	s_waitcnt lgkmcnt(1)
	s_nop 0
	v_pk_mul_f32 v[22:23], v[22:23], v[74:75]
	s_waitcnt lgkmcnt(0)
	s_nop 0
	v_pk_mul_f32 v[18:19], v[18:19], v[80:81]
	v_pk_mul_f32 v[28:29], v[28:29], v[64:65]
	v_pk_mul_f32 v[24:25], v[24:25], v[68:69]
	v_pk_mul_f32 v[20:21], v[20:21], v[72:73]
	v_pk_mul_f32 v[16:17], v[16:17], v[78:79]
	v_pk_mul_f32 v[14:15], v[14:15], v[66:67]
	v_pk_mul_f32 v[10:11], v[10:11], v[70:71]
	v_pk_mul_f32 v[6:7], v[6:7], v[74:75]
	v_pk_mul_f32 v[2:3], v[2:3], v[80:81]
	v_pk_mul_f32 v[12:13], v[12:13], v[64:65]
	v_pk_mul_f32 v[8:9], v[8:9], v[68:69]
	v_pk_mul_f32 v[4:5], v[4:5], v[72:73]
	v_pk_mul_f32 v[0:1], v[0:1], v[78:79]
.LBB0_747:
	v_add_f32_e32 v64, v48, v49
	v_add_f32_e32 v64, v50, v64
	v_add_f32_e32 v64, v51, v64
	v_add_f32_e32 v64, v52, v64
	v_add_f32_e32 v64, v53, v64
	v_add_f32_e32 v64, v54, v64
	v_add_f32_e32 v64, v55, v64
	v_add_f32_e32 v64, v56, v64
	v_add_f32_e32 v64, v57, v64
	v_add_f32_e32 v64, v58, v64
	v_add_f32_e32 v64, v59, v64
	v_add_f32_e32 v64, v60, v64
	v_add_f32_e32 v64, v61, v64
	v_add_f32_e32 v64, v62, v64
	v_add_f32_e32 v64, v63, v64
	v_add_f32_e32 v64, v32, v64
	v_add_f32_e32 v64, v33, v64
	v_add_f32_e32 v64, v34, v64
	v_add_f32_e32 v64, v35, v64
	v_add_f32_e32 v64, v36, v64
	v_add_f32_e32 v64, v37, v64
	v_add_f32_e32 v64, v38, v64
	v_add_f32_e32 v64, v39, v64
	v_add_f32_e32 v64, v40, v64
	v_add_f32_e32 v64, v41, v64
	v_add_f32_e32 v64, v42, v64
	v_add_f32_e32 v64, v43, v64
	v_add_f32_e32 v64, v44, v64
	v_add_f32_e32 v64, v45, v64
	s_cmp_lg_u32 0, -1
	v_add_f32_e32 v64, v46, v64
	s_cselect_b32 s2, 0, 0
	v_add_f32_e32 v64, v47, v64
	s_addk_i32 s2, 0x6000
	v_add_f32_e64 v64, v76, v64
	v_cvt_pk_bf16_f32 v32, v32, v33
	v_add3_u32 v65, v218, s2, v216
	v_cvt_pk_bf16_f32 v48, v48, v49
	v_cvt_pk_bf16_f32 v49, v50, v51
	v_cvt_pk_bf16_f32 v50, v52, v53
	v_cvt_pk_bf16_f32 v51, v54, v55
	v_cvt_pk_bf16_f32 v52, v56, v57
	v_cvt_pk_bf16_f32 v53, v58, v59
	v_cvt_pk_bf16_f32 v54, v60, v61
	v_cvt_pk_bf16_f32 v55, v62, v63
	v_cvt_pk_bf16_f32 v33, v34, v35
	v_cvt_pk_bf16_f32 v34, v36, v37
	v_cvt_pk_bf16_f32 v35, v38, v39
	v_cvt_pk_bf16_f32 v36, v40, v41
	v_cvt_pk_bf16_f32 v37, v42, v43
	v_cvt_pk_bf16_f32 v38, v44, v45
	v_cvt_pk_bf16_f32 v39, v46, v47
	v_add3_u32 v65, v65, v217, s38
	ds_read_b64_tr_b16 v[40:41],v65 offset:0
	ds_read_b64_tr_b16 v[42:43],v65 offset:512
	ds_read_b64_tr_b16 v[44:45],v65 offset:1024
	ds_read_b64_tr_b16 v[46:47],v65 offset:1536
	ds_read_b64_tr_b16 v[56:57],v65 offset:2048
	ds_read_b64_tr_b16 v[58:59],v65 offset:2560
	ds_read_b64_tr_b16 v[60:61],v65 offset:3072
	ds_read_b64_tr_b16 v[62:63],v65 offset:3584
	s_waitcnt lgkmcnt(0)
	s_nop 0
	v_mfma_f32_32x32x16_bf16 v[16:31], v[48:51], v[40:43], v[16:31]
	ds_read_b64_tr_b16 v[40:41],v65 offset:4096
	ds_read_b64_tr_b16 v[42:43],v65 offset:4608
	v_mfma_f32_32x32x16_bf16 v[16:31], v[52:55], v[44:47], v[16:31]
	ds_read_b64_tr_b16 v[44:45],v65 offset:5120
	ds_read_b64_tr_b16 v[46:47],v65 offset:5632
	v_mfma_f32_32x32x16_bf16 v[16:31], v[32:35], v[56:59], v[16:31]
	ds_read_b64_tr_b16 v[56:57],v65 offset:6144
	ds_read_b64_tr_b16 v[58:59],v65 offset:6656
	v_mfma_f32_32x32x16_bf16 v[16:31], v[36:39], v[60:63], v[16:31]
	ds_read_b64_tr_b16 v[60:61],v65 offset:7168
	ds_read_b64_tr_b16 v[62:63],v65 offset:7680
	s_waitcnt lgkmcnt(0)
	s_nop 0
	v_mfma_f32_32x32x16_bf16 v[0:15], v[48:51], v[40:43], v[0:15]
	v_cmp_gt_u32_e32 vcc, 32, v199
	s_nop 0
	v_mfma_f32_32x32x16_bf16 v[0:15], v[52:55], v[44:47], v[0:15]
	v_mfma_f32_32x32x16_bf16 v[0:15], v[32:35], v[56:59], v[0:15]
	v_mov_b32_e64 v32, v64
	s_nop 1
	v_permlane32_swap_b32_e32 v64, v32
	v_mfma_f32_32x32x16_bf16 v[0:15], v[36:39], v[60:63], v[0:15]
	s_and_saveexec_b64 s[2:3], vcc
	s_cbranch_execz .LBB0_717
	v_add_f32_e64 v32, v64, v32
	ds_write_b32 v235, v32 offset:49280
	s_branch .LBB0_717

.LBB0_750:
	s_lshl_b32 s18, s96, 6
	s_addk_i32 s18, 0x7b
	v_add_u32_e32 v114, s18, v236
	s_lshl_b32 s18, s40, 2
	s_sub_i32 s23, 0, s18
	s_add_i32 s40, s96, 4
	s_lshl_b64 s[18:19], s[96:97], 17
	s_add_u32 s18, s14, s18
	s_addc_u32 s19, s15, s19
	s_lshl_b64 s[14:15], s[16:17], 1
	s_add_u32 s14, s14, s18
	v_mov_b32_e32 v205, v97
	s_addc_u32 s15, s15, s19
	v_subrev_u32_e64 v212, s45, v114
	v_lshl_add_u64 v[114:115], s[14:15], 0, v[204:205]
	s_lshl_b32 s14, s41, 9
	s_nop 0
	s_and_b32 s14, s14, 0x18000
	v_lshl_or_b32 v118, v241, 11, s14
	s_lshl_b32 s14, s96, 8
	s_add_i32 s14, s14, 0
	s_add_i32 s14, s14, 0x15100
	s_lshl_b64 s[4:5], s[4:5], 1
	s_add_u32 s4, s70, s4
	s_addc_u32 s5, s71, s5
	v_mov_b32_e32 v119, v97
	s_add_u32 s4, s4, s18
	s_nop 0
	v_lshl_add_u64 v[114:115], v[114:115], 0, v[118:119]
	s_addc_u32 s5, s5, s19
	s_nop 0
	v_cmp_gt_u32_e64 s[2:3], 32, v199
	v_lshl_add_u64 v[204:205], s[70:71], 0, v[114:115]
	v_lshl_add_u32 v213, v215, 4, s14
	v_lshl_add_u64 v[206:207], s[4:5], 0, v[96:97]
.LBB0_751:
	v_add_u32_e64 v96, s22, v239
	ds_read_b64_tr_b16 v[194:195], v96 offset:24576
	ds_read_b64_tr_b16 v[196:197], v96 offset:25088
	s_waitcnt lgkmcnt(2)
	s_nop 0
	v_mfma_f32_32x32x16_bf16 v[48:63], v[158:161], v[110:113], v[48:63]
	v_add_f32_e32 v114, v80, v81
	v_add_f32_e32 v114, v82, v114
	v_add_f32_e32 v114, v83, v114
	v_add_f32_e32 v114, v84, v114
	v_add_f32_e64 v114, v85, v114
	v_cvt_pk_bf16_f32 v126, v80, v81
	v_cvt_pk_bf16_f32 v127, v82, v83
	ds_read_b64_tr_b16 v[190:191], v96 offset:28672
	ds_read_b64_tr_b16 v[192:193], v96 offset:29184
	v_mfma_f32_32x32x16_bf16 v[32:47], v[146:149], v[110:113], v[32:47]
	v_add_f32_e32 v80, v86, v114
	v_add_f32_e32 v80, v87, v80
	v_add_f32_e32 v80, v88, v80
	v_add_f32_e32 v80, v89, v80
	v_cvt_pk_bf16_f32 v128, v84, v85
	v_cvt_pk_bf16_f32 v129, v86, v87
	ds_read_b64_tr_b16 v[186:187], v96 offset:25600
	ds_read_b64_tr_b16 v[188:189], v96 offset:26112
	v_mfma_f32_32x32x16_bf16 v[48:63], v[154:157], v[106:109], v[48:63]
	v_add_f32_e32 v80, v90, v80
	v_add_f32_e32 v80, v91, v80
	v_add_f32_e32 v80, v92, v80
	v_add_f32_e32 v80, v93, v80
	v_cvt_pk_bf16_f32 v122, v88, v89
	v_cvt_pk_bf16_f32 v123, v90, v91
	ds_read_b64_tr_b16 v[182:183], v96 offset:29696
	ds_read_b64_tr_b16 v[184:185], v96 offset:30208
	v_mfma_f32_32x32x16_bf16 v[32:47], v[142:145], v[106:109], v[32:47]
	v_add_f32_e32 v80, v94, v80
	v_add_f32_e32 v80, v95, v80
	v_add_f32_e32 v80, v64, v80
	v_add_f32_e32 v80, v65, v80
	v_cvt_pk_bf16_f32 v124, v92, v93
	v_cvt_pk_bf16_f32 v125, v94, v95
	ds_read_b64_tr_b16 v[178:179], v96 offset:26624
	ds_read_b64_tr_b16 v[180:181], v96 offset:27136
	v_mfma_f32_32x32x16_bf16 v[48:63], v[150:153], v[102:105], v[48:63]
	v_add_f32_e32 v80, v66, v80
	v_add_f32_e32 v80, v67, v80
	v_add_f32_e32 v80, v68, v80
	v_add_f32_e32 v80, v69, v80
	v_cvt_pk_bf16_f32 v118, v64, v65
	v_cvt_pk_bf16_f32 v119, v66, v67
	ds_read_b64_tr_b16 v[174:175], v96 offset:30720
	ds_read_b64_tr_b16 v[176:177], v96 offset:31232
	v_mfma_f32_32x32x16_bf16 v[32:47], v[138:141], v[102:105], v[32:47]
	v_add_f32_e32 v64, v70, v80
	v_add_f32_e32 v64, v71, v64
	v_add_f32_e32 v64, v72, v64
	v_add_f32_e32 v64, v73, v64
	v_cvt_pk_bf16_f32 v120, v68, v69
	v_cvt_pk_bf16_f32 v121, v70, v71
	ds_read_b64_tr_b16 v[170:171], v96 offset:27648
	ds_read_b64_tr_b16 v[172:173], v96 offset:28160
	v_mfma_f32_32x32x16_bf16 v[48:63], v[134:137], v[98:101], v[48:63]
	v_add_f32_e32 v64, v74, v64
	v_add_f32_e32 v64, v75, v64
	v_add_f32_e32 v64, v76, v64
	v_add_f32_e32 v64, v77, v64
	v_cvt_pk_bf16_f32 v114, v72, v73
	v_cvt_pk_bf16_f32 v115, v74, v75
	ds_read_b64_tr_b16 v[166:167], v96 offset:31744
	ds_read_b64_tr_b16 v[168:169], v96 offset:32256
	v_mfma_f32_32x32x16_bf16 v[32:47], v[130:133], v[98:101], v[32:47]
	v_add_f32_e32 v64, v78, v64
	v_add_f32_e32 v64, v79, v64
	v_add_f32_e64 v80, 0, v64
	v_cvt_pk_bf16_f32 v116, v76, v77
	v_cvt_pk_bf16_f32 v117, v78, v79
	s_waitcnt lgkmcnt(14)
	s_nop 0
	ds_read_b128 v[64:67], v213
	ds_read_b128 v[68:71], v213 offset:32
	ds_read_b128 v[82:85], v213 offset:128
	ds_read_b128 v[86:89], v213 offset:160
	ds_read_b128 v[72:75], v213 offset:64
	ds_read_b128 v[76:79], v213 offset:96
	ds_read_b128 v[90:93], v213 offset:192
	ds_read_b128 v[162:165], v213 offset:224
	s_add_i32 s22, s40, -1
	s_cmp_ge_u32 s22, s39
	s_cselect_b64 s[14:15], -1, 0
	s_and_b64 vcc, exec, s[14:15]
	v_lshl_add_u64 v[210:211], v[206:207], 0, s[12:13]
	s_cbranch_vccnz .LBB0_753
	s_nop 0
	s_mov_b64 s[4:5], 0x16e60000
	s_add_i32 s16, s38, s30
	s_nop 0
	v_lshl_add_u64 v[94:95], v[210:211], 0, s[4:5]
	s_mov_b32 s4, m0
	s_mov_b32 m0, s16
	s_nop 0
	s_nop 0
	global_load_lds_dwordx4 v[94:95], off
	s_mov_b32 m0, s4
.LBB0_753:
	s_nop 0
	v_lshl_add_u64 v[208:209], v[204:205], 0, s[12:13]
	s_mov_b64 s[4:5], 0x1ee20000
	v_lshl_add_u64 v[94:95], v[208:209], 0, s[4:5]
	s_add_i32 s4, s46, s31
	s_mov_b32 s5, m0
	s_mov_b32 m0, s4
	s_nop 0
	global_load_lds_dwordx4 v[94:95], off
	s_mov_b32 m0, s5
	s_add_i32 s20, s23, s40
	s_add_i32 s4, s20, -4
	s_cmp_lt_i32 s4, 0
	s_cbranch_scc1 .LBB0_755
	s_nop 0
	v_add_u32_e32 v94, 0xffffffa5, v212
	v_add_u32_e32 v81, 0xffffff85, v212
	v_cmp_le_i32_e32 vcc, v94, v237
	s_nop 1
	v_cndmask_b32_e32 v32, v232, v32, vcc
	v_cmp_lt_i32_e32 vcc, v81, v237
	s_nop 1
	v_cndmask_b32_e32 v49, v232, v49, vcc
	v_cmp_le_i32_e32 vcc, v81, v237
	s_nop 0
	v_add_u32_e32 v81, 0xffffffa6, v212
	s_nop 0
	v_cndmask_b32_e32 v48, v232, v48, vcc
	v_cmp_le_i32_e32 vcc, v81, v237
	s_nop 0
	v_add_u32_e32 v81, 0xffffff87, v212
	s_nop 0
	v_cndmask_b32_e32 v33, v232, v33, vcc
	v_cmp_le_i32_e32 vcc, v81, v237
	s_nop 0
	v_add_u32_e32 v81, 0xffffffa7, v212
	s_nop 0
	v_cndmask_b32_e32 v50, v232, v50, vcc
	v_cmp_le_i32_e32 vcc, v81, v237
	s_nop 0
	v_add_u32_e32 v81, 0xffffff88, v212
	s_nop 0
	v_cndmask_b32_e32 v34, v232, v34, vcc
	v_cmp_le_i32_e32 vcc, v81, v237
	s_nop 0
	v_add_u32_e32 v81, 0xffffffa8, v212
	s_nop 0
	v_cndmask_b32_e32 v51, v232, v51, vcc
	v_cmp_le_i32_e32 vcc, v81, v237
	s_nop 0
	v_add_u32_e32 v81, 0xffffff8d, v212
	s_nop 0
	v_cndmask_b32_e32 v35, v232, v35, vcc
	v_cmp_le_i32_e32 vcc, v81, v237
	s_nop 0
	v_add_u32_e32 v81, 0xffffffad, v212
	s_nop 0
	v_cndmask_b32_e32 v52, v232, v52, vcc
	v_cmp_le_i32_e32 vcc, v81, v237
	s_nop 0
	v_add_u32_e32 v81, 0xffffff8e, v212
	s_nop 0
	v_cndmask_b32_e32 v36, v232, v36, vcc
	v_cmp_le_i32_e32 vcc, v81, v237
	s_nop 0
	v_add_u32_e32 v81, 0xffffffae, v212
	s_nop 0
	v_cndmask_b32_e32 v53, v232, v53, vcc
	v_cmp_le_i32_e32 vcc, v81, v237
	s_nop 0
	v_add_u32_e32 v81, 0xffffff8f, v212
	s_nop 0
	v_cndmask_b32_e32 v37, v232, v37, vcc
	v_cmp_le_i32_e32 vcc, v81, v237
	s_nop 0
	v_add_u32_e32 v81, 0xffffffaf, v212
	s_nop 0
	v_cndmask_b32_e32 v54, v232, v54, vcc
	v_cmp_le_i32_e32 vcc, v81, v237
	s_nop 0
	v_add_u32_e32 v81, 0xffffff90, v212
	s_nop 0
	v_cndmask_b32_e32 v38, v232, v38, vcc
	v_cmp_le_i32_e32 vcc, v81, v237
	s_nop 0
	v_add_u32_e32 v81, 0xffffffb0, v212
	s_nop 0
	v_cndmask_b32_e32 v55, v232, v55, vcc
	v_cmp_le_i32_e32 vcc, v81, v237
	s_nop 0
	v_add_u32_e32 v81, 0xffffff95, v212
	s_nop 0
	v_cndmask_b32_e32 v39, v232, v39, vcc
	v_cmp_le_i32_e32 vcc, v81, v237
	s_nop 0
	v_add_u32_e32 v81, 0xffffffb5, v212
	s_nop 0
	v_cndmask_b32_e32 v56, v232, v56, vcc
	v_cmp_le_i32_e32 vcc, v81, v237
	s_nop 0
	v_add_u32_e32 v81, 0xffffff96, v212
	s_nop 0
	v_cndmask_b32_e32 v40, v232, v40, vcc
	v_cmp_le_i32_e32 vcc, v81, v237
	s_nop 0
	v_add_u32_e32 v81, 0xffffffb6, v212
	s_nop 0
	v_cndmask_b32_e32 v57, v232, v57, vcc
	v_cmp_le_i32_e32 vcc, v81, v237
	s_nop 0
	v_add_u32_e32 v81, 0xffffff97, v212
	s_nop 0
	v_cndmask_b32_e32 v41, v232, v41, vcc
	v_cmp_le_i32_e32 vcc, v81, v237
	s_nop 0
	v_add_u32_e32 v81, 0xffffffb7, v212
	s_nop 0
	v_cndmask_b32_e32 v58, v232, v58, vcc
	v_cmp_le_i32_e32 vcc, v81, v237
	s_nop 0
	v_add_u32_e32 v81, 0xffffff98, v212
	s_nop 0
	v_cndmask_b32_e32 v42, v232, v42, vcc
	v_cmp_le_i32_e32 vcc, v81, v237
	s_nop 0
	v_add_u32_e32 v81, 0xffffffb8, v212
	s_nop 0
	v_cndmask_b32_e32 v59, v232, v59, vcc
	v_cmp_le_i32_e32 vcc, v81, v237
	s_nop 0
	v_add_u32_e32 v81, 0xffffff9d, v212
	s_nop 0
	v_cndmask_b32_e32 v43, v232, v43, vcc
	v_cmp_le_i32_e32 vcc, v81, v237
	s_nop 0
	v_add_u32_e32 v81, 0xffffffbd, v212
	s_nop 0
	v_cndmask_b32_e32 v60, v232, v60, vcc
	v_cmp_le_i32_e32 vcc, v81, v237
	s_nop 0
	v_add_u32_e32 v81, 0xffffff9e, v212
	s_nop 0
	v_cndmask_b32_e32 v44, v232, v44, vcc
	v_cmp_le_i32_e32 vcc, v81, v237
	s_nop 0
	v_add_u32_e32 v81, 0xffffffbe, v212
	s_nop 0
	v_cndmask_b32_e32 v61, v232, v61, vcc
	v_cmp_le_i32_e32 vcc, v81, v237
	s_nop 0
	v_add_u32_e32 v81, 0xffffff9f, v212
	s_nop 0
	v_cndmask_b32_e32 v45, v232, v45, vcc
	v_cmp_le_i32_e32 vcc, v81, v237
	s_nop 0
	v_add_u32_e32 v81, 0xffffffbf, v212
	s_nop 0
	v_cndmask_b32_e32 v62, v232, v62, vcc
	v_cmp_le_i32_e32 vcc, v81, v237
	s_nop 0
	v_add_u32_e32 v81, 0xffffffa0, v212
	s_nop 0
	v_cndmask_b32_e32 v46, v232, v46, vcc
	v_cmp_le_i32_e32 vcc, v81, v237
	v_subrev_u32_e32 v81, 64, v212
	s_nop 0
	v_cndmask_b32_e32 v63, v232, v63, vcc
	v_cmp_le_i32_e32 vcc, v81, v237
	s_nop 1
	v_cndmask_b32_e32 v47, v232, v47, vcc

.LBB0_756:
	v_mfma_f32_32x32x16_bf16 v[16:31], v[126:129], v[194:197], v[16:31]
	v_exp_f32_e32 v48, v48
	v_exp_f32_e32 v49, v49
	v_exp_f32_e64 v50, v50
	v_exp_f32_e32 v51, v51
	s_waitcnt lgkmcnt(14)
	v_mfma_f32_32x32x16_bf16 v[0:15], v[126:129], v[190:193], v[0:15]
	v_exp_f32_e32 v52, v52
	v_exp_f32_e32 v53, v53
	v_exp_f32_e32 v54, v54
	v_exp_f32_e32 v55, v55
	v_add_u32_e64 v80, s46, v238
	ds_read_b128 v[158:161], v80
	ds_read_b128 v[146:149], v80 offset:512
	v_mfma_f32_32x32x16_bf16 v[16:31], v[122:125], v[186:189], v[16:31]
	v_exp_f32_e32 v56, v56
	v_exp_f32_e32 v57, v57
	v_exp_f32_e32 v58, v58
	v_exp_f32_e32 v59, v59
	ds_read_b128 v[154:157], v80 offset:2048
	ds_read_b128 v[142:145], v80 offset:2560
	v_mfma_f32_32x32x16_bf16 v[0:15], v[122:125], v[182:185], v[0:15]
	v_exp_f32_e32 v60, v60
	v_exp_f32_e32 v61, v61
	v_exp_f32_e32 v62, v62
	v_exp_f32_e32 v63, v63
	ds_read_b128 v[150:153], v80 offset:4096
	ds_read_b128 v[138:141], v80 offset:4608
	v_mfma_f32_32x32x16_bf16 v[16:31], v[118:121], v[178:181], v[16:31]
	v_exp_f32_e32 v32, v32
	v_exp_f32_e32 v33, v33
	v_exp_f32_e32 v34, v34
	v_exp_f32_e32 v35, v35
	ds_read_b128 v[134:137], v80 offset:6144
	ds_read_b128 v[130:133], v80 offset:6656
	s_waitcnt lgkmcnt(14)
	s_nop 0
	v_mfma_f32_32x32x16_bf16 v[0:15], v[118:121], v[174:177], v[0:15]
	v_exp_f32_e32 v36, v36
	v_exp_f32_e32 v37, v37
	v_exp_f32_e32 v38, v38
	v_exp_f32_e32 v39, v39
	v_mfma_f32_32x32x16_bf16 v[16:31], v[114:117], v[170:173], v[16:31]
	v_exp_f32_e32 v40, v40
	v_exp_f32_e32 v41, v41
	v_exp_f32_e32 v42, v42
	v_exp_f32_e32 v43, v43
	v_mfma_f32_32x32x16_bf16 v[0:15], v[114:117], v[166:169], v[0:15]
	v_exp_f32_e32 v44, v44
	v_exp_f32_e32 v45, v45
	v_exp_f32_e32 v46, v46
	v_exp_f32_e32 v47, v47
	s_mov_b64 s[16:17], -1
	s_and_b64 vcc, exec, s[14:15]
	s_cbranch_vccz .LBB0_793
	s_add_i32 s16, s40, -2
	s_cmp_ge_u32 s16, s39
	s_mov_b64 s[16:17], -1
	s_cbranch_scc0 .LBB0_759
	s_waitcnt vmcnt(0) lgkmcnt(0)
	s_barrier
	s_mov_b64 s[16:17], 0

.LBB0_763:
	s_waitcnt lgkmcnt(0)
	ds_read_b128 v[166:169], v219 offset:49248
	ds_read_b128 v[170:173], v219 offset:49216
	ds_read_b128 v[174:177], v219 offset:49184
	ds_read_b128 v[178:181], v219 offset:49152
	s_waitcnt lgkmcnt(3)
	s_nop 0
	v_pk_mul_f32 v[30:31], v[30:31], v[168:169]
	s_waitcnt lgkmcnt(2)
	s_nop 0
	v_pk_mul_f32 v[26:27], v[26:27], v[172:173]
	s_waitcnt lgkmcnt(1)
	s_nop 0
	v_pk_mul_f32 v[22:23], v[22:23], v[176:177]
	s_waitcnt lgkmcnt(0)
	s_nop 0
	v_pk_mul_f32 v[18:19], v[18:19], v[180:181]
	v_pk_mul_f32 v[28:29], v[28:29], v[166:167]
	v_pk_mul_f32 v[24:25], v[24:25], v[170:171]
	v_pk_mul_f32 v[20:21], v[20:21], v[174:175]
	v_pk_mul_f32 v[16:17], v[16:17], v[178:179]
	v_pk_mul_f32 v[14:15], v[14:15], v[168:169]
	v_pk_mul_f32 v[10:11], v[10:11], v[172:173]
	v_pk_mul_f32 v[6:7], v[6:7], v[176:177]
	v_pk_mul_f32 v[2:3], v[2:3], v[180:181]
	v_pk_mul_f32 v[12:13], v[12:13], v[166:167]
	v_pk_mul_f32 v[8:9], v[8:9], v[170:171]
	v_pk_mul_f32 v[4:5], v[4:5], v[174:175]
	v_pk_mul_f32 v[0:1], v[0:1], v[178:179]
.LBB0_764:
	v_pk_add_f32 v[80:81], v[64:65], v[202:203] op_sel_hi:[1,0] neg_lo:[0,1] neg_hi:[0,1]
	s_waitcnt lgkmcnt(13)
	s_nop 0
	v_pk_add_f32 v[64:65], v[82:83], v[202:203] op_sel_hi:[1,0] neg_lo:[0,1] neg_hi:[0,1]
	v_pk_add_f32 v[82:83], v[66:67], v[202:203] op_sel_hi:[1,0] neg_lo:[0,1] neg_hi:[0,1]
	v_pk_add_f32 v[66:67], v[84:85], v[202:203] op_sel_hi:[1,0] neg_lo:[0,1] neg_hi:[0,1]
	v_pk_add_f32 v[84:85], v[68:69], v[202:203] op_sel_hi:[1,0] neg_lo:[0,1] neg_hi:[0,1]
	s_waitcnt lgkmcnt(12)
	s_nop 0
	v_pk_add_f32 v[68:69], v[86:87], v[202:203] op_sel_hi:[1,0] neg_lo:[0,1] neg_hi:[0,1]
	v_pk_add_f32 v[86:87], v[70:71], v[202:203] op_sel_hi:[1,0] neg_lo:[0,1] neg_hi:[0,1]
	v_pk_add_f32 v[70:71], v[88:89], v[202:203] op_sel_hi:[1,0] neg_lo:[0,1] neg_hi:[0,1]
	s_waitcnt lgkmcnt(11)
	s_nop 0
	v_pk_add_f32 v[88:89], v[72:73], v[202:203] op_sel_hi:[1,0] neg_lo:[0,1] neg_hi:[0,1]
	s_waitcnt lgkmcnt(9)
	s_nop 0
	v_pk_add_f32 v[72:73], v[90:91], v[202:203] op_sel_hi:[1,0] neg_lo:[0,1] neg_hi:[0,1]
	v_pk_add_f32 v[90:91], v[74:75], v[202:203] op_sel_hi:[1,0] neg_lo:[0,1] neg_hi:[0,1]
	v_pk_add_f32 v[74:75], v[92:93], v[202:203] op_sel_hi:[1,0] neg_lo:[0,1] neg_hi:[0,1]
	v_pk_add_f32 v[92:93], v[76:77], v[202:203] op_sel_hi:[1,0] neg_lo:[0,1] neg_hi:[0,1]
	s_waitcnt lgkmcnt(8)
	s_nop 0
	v_pk_add_f32 v[76:77], v[162:163], v[202:203] op_sel_hi:[1,0] neg_lo:[0,1] neg_hi:[0,1]
	v_pk_add_f32 v[94:95], v[78:79], v[202:203] op_sel_hi:[1,0] neg_lo:[0,1] neg_hi:[0,1]
	v_pk_add_f32 v[78:79], v[164:165], v[202:203] op_sel_hi:[1,0] neg_lo:[0,1] neg_hi:[0,1]
	v_add_u32_e64 v164, s38, v239
	ds_read_b64_tr_b16 v[190:191], v164 offset:24576
	ds_read_b64_tr_b16 v[192:193], v164 offset:25088
	s_waitcnt lgkmcnt(9)
	s_nop 0
	v_mfma_f32_32x32x16_bf16 v[80:95], v[158:161], v[110:113], v[80:95]
	v_add_f32_e32 v114, v48, v49
	v_add_f32_e32 v114, v50, v114
	v_add_f32_e32 v114, v51, v114
	v_add_f32_e32 v114, v52, v114
	v_add_f32_e64 v114, v53, v114
	v_cvt_pk_bf16_f32 v126, v48, v49
	v_cvt_pk_bf16_f32 v127, v50, v51
	ds_read_b64_tr_b16 v[186:187], v164 offset:28672
	ds_read_b64_tr_b16 v[188:189], v164 offset:29184
	s_waitcnt lgkmcnt(10)
	s_nop 0
	v_mfma_f32_32x32x16_bf16 v[64:79], v[146:149], v[110:113], v[64:79]
	v_add_f32_e32 v114, v54, v114
	v_add_f32_e32 v114, v55, v114
	v_add_f32_e32 v114, v56, v114
	v_add_f32_e32 v114, v57, v114
	v_cvt_pk_bf16_f32 v128, v52, v53
	v_cvt_pk_bf16_f32 v129, v54, v55
	ds_read_b64_tr_b16 v[182:183], v164 offset:25600
	ds_read_b64_tr_b16 v[184:185], v164 offset:26112
	s_waitcnt lgkmcnt(11)
	s_nop 0
	v_mfma_f32_32x32x16_bf16 v[80:95], v[154:157], v[106:109], v[80:95]
	v_add_f32_e32 v114, v58, v114
	v_add_f32_e32 v114, v59, v114
	v_add_f32_e32 v114, v60, v114
	v_add_f32_e32 v114, v61, v114
	v_cvt_pk_bf16_f32 v122, v56, v57
	v_cvt_pk_bf16_f32 v123, v58, v59
	ds_read_b64_tr_b16 v[178:179], v164 offset:29696
	ds_read_b64_tr_b16 v[180:181], v164 offset:30208
	s_waitcnt lgkmcnt(12)
	s_nop 0
	v_mfma_f32_32x32x16_bf16 v[64:79], v[142:145], v[106:109], v[64:79]
	v_add_f32_e32 v114, v62, v114
	v_add_f32_e32 v114, v63, v114
	v_add_f32_e32 v114, v32, v114
	v_add_f32_e32 v114, v33, v114
	v_cvt_pk_bf16_f32 v124, v60, v61
	v_cvt_pk_bf16_f32 v125, v62, v63
	ds_read_b64_tr_b16 v[174:175], v164 offset:26624
	ds_read_b64_tr_b16 v[176:177], v164 offset:27136
	s_waitcnt lgkmcnt(13)
	s_nop 0
	v_mfma_f32_32x32x16_bf16 v[80:95], v[150:153], v[102:105], v[80:95]
	v_add_f32_e32 v114, v34, v114
	v_add_f32_e32 v114, v35, v114
	v_add_f32_e32 v114, v36, v114
	v_add_f32_e32 v114, v37, v114
	v_cvt_pk_bf16_f32 v118, v32, v33
	v_cvt_pk_bf16_f32 v119, v34, v35
	ds_read_b64_tr_b16 v[170:171], v164 offset:30720
	ds_read_b64_tr_b16 v[172:173], v164 offset:31232
	s_waitcnt lgkmcnt(14)
	s_nop 0
	v_mfma_f32_32x32x16_bf16 v[64:79], v[138:141], v[102:105], v[64:79]
	v_add_f32_e32 v114, v38, v114
	v_add_f32_e32 v114, v39, v114
	v_add_f32_e32 v114, v40, v114
	v_add_f32_e32 v114, v41, v114
	v_cvt_pk_bf16_f32 v120, v36, v37
	v_cvt_pk_bf16_f32 v121, v38, v39
	ds_read_b64_tr_b16 v[166:167], v164 offset:27648
	ds_read_b64_tr_b16 v[168:169], v164 offset:28160
	s_waitcnt lgkmcnt(14)
	s_nop 0
	v_mfma_f32_32x32x16_bf16 v[80:95], v[134:137], v[98:101], v[80:95]
	v_add_f32_e32 v114, v42, v114
	v_add_f32_e32 v114, v43, v114
	v_add_f32_e32 v114, v44, v114
	v_add_f32_e32 v194, v45, v114
	v_cvt_pk_bf16_f32 v114, v40, v41
	v_cvt_pk_bf16_f32 v115, v42, v43
	ds_read_b64_tr_b16 v[162:163], v164 offset:31744
	ds_read_b64_tr_b16 v[164:165], v164 offset:32256
	v_mfma_f32_32x32x16_bf16 v[64:79], v[130:133], v[98:101], v[64:79]
	v_add_f32_e32 v116, v46, v194
	v_add_f32_e32 v116, v47, v116
	v_add_f32_e64 v194, 0, v116
	v_cvt_pk_bf16_f32 v116, v44, v45
	v_cvt_pk_bf16_f32 v117, v46, v47
	s_add_i32 s4, s40, -2
	s_cmp_lt_u32 s4, s39
	s_cselect_b64 s[18:19], -1, 0
	s_cmp_ge_u32 s4, s39
	s_cbranch_scc1 .LBB0_766
	s_nop 0
	ds_read_b128 v[48:51], v213 offset:256
	ds_read_b128 v[52:55], v213 offset:288
	ds_read_b128 v[32:35], v213 offset:384
	ds_read_b128 v[36:39], v213 offset:416
	ds_read_b128 v[56:59], v213 offset:320
	ds_read_b128 v[60:63], v213 offset:352
	ds_read_b128 v[40:43], v213 offset:448
	ds_read_b128 v[44:47], v213 offset:480
.LBB0_766:
	s_cmp_ge_u32 s40, s39
	s_cselect_b64 s[16:17], -1, 0
	s_and_b64 vcc, exec, s[16:17]
	s_cbranch_vccnz .LBB0_768
	s_mov_b64 s[48:49], 0x16e80000
	s_add_i32 s4, s46, s30
	s_nop 0
	v_lshl_add_u64 v[196:197], v[210:211], 0, s[48:49]
	s_mov_b32 s5, m0
	s_mov_b32 m0, s4
	s_nop 0
	s_nop 0
	global_load_lds_dwordx4 v[196:197], off
	s_mov_b32 m0, s5
.LBB0_768:
	s_nop 0
	s_add_i32 s4, s46, 0x2000
	s_cmpk_lg_i32 s46, 0x4000
	s_nop 0
	v_cndmask_b32_e64 v195, 0, 1, s[18:19]
	s_cselect_b32 s38, s4, 0
	s_nop 0
	v_cmp_ne_u32_e64 s[4:5], 1, v195
	s_andn2_b64 vcc, exec, s[18:19]
	s_cbranch_vccnz .LBB0_770
	s_mov_b64 s[48:49], 0x1ee40000
	s_add_i32 s18, s38, s31
	s_nop 0
	v_lshl_add_u64 v[196:197], v[208:209], 0, s[48:49]
	s_mov_b32 s19, m0
	s_mov_b32 m0, s18
	s_nop 0
	s_nop 0
	global_load_lds_dwordx4 v[196:197], off
	s_mov_b32 m0, s19

.LBB0_772:
	v_add_f32_e32 v240, v96, v194
	v_max_f32_e32 v96, v81, v81
	v_max_f32_e32 v194, v80, v80
	v_max_f32_e32 v96, v194, v96
	v_max3_f32 v194, v82, v83, v65
	v_max3_f32 v96, v96, v64, v66
	v_max3_f32 v96, v96, v67, v84
	v_max3_f32 v194, v194, v86, v87
	v_max3_f32 v96, v96, v85, v68
	v_max3_f32 v194, v194, v70, v71
	v_max3_f32 v96, v96, v69, v88
	v_max3_f32 v194, v194, v90, v91
	v_max3_f32 v96, v96, v89, v72
	v_max3_f32 v194, v194, v74, v75
	v_max3_f32 v96, v96, v73, v92
	v_max3_f32 v194, v194, v94, v95
	v_max3_f32 v96, v96, v93, v76
	v_max3_f32 v194, v194, v78, v79
	v_max3_f32 v96, v96, v77, v194
	v_mov_b32_e32 v194, v96
	s_nop 1
	v_permlane32_swap_b32_e32 v96, v194
	v_max_f32_e32 v194, v194, v194
	v_max_f32_e64 v96, v96, v96
	v_max_f32_e32 v96, v96, v194
	v_cmp_lt_f32_e32 vcc, s51, v96
	s_cmp_lg_u64 vcc, 0
	s_cselect_b64 s[18:19], -1, 0
	s_cbranch_vccnz .LBB0_800
	s_and_b64 vcc, exec, s[4:5]
	s_cbranch_vccnz .LBB0_775
.LBB0_774:
	s_waitcnt lgkmcnt(2)
	v_pk_add_f32 v[62:63], v[62:63], v[202:203] op_sel_hi:[1,0] neg_lo:[0,1] neg_hi:[0,1]
	v_pk_add_f32 v[60:61], v[60:61], v[202:203] op_sel_hi:[1,0] neg_lo:[0,1] neg_hi:[0,1]
	v_pk_add_f32 v[58:59], v[58:59], v[202:203] op_sel_hi:[1,0] neg_lo:[0,1] neg_hi:[0,1]
	v_pk_add_f32 v[56:57], v[56:57], v[202:203] op_sel_hi:[1,0] neg_lo:[0,1] neg_hi:[0,1]
	v_pk_add_f32 v[54:55], v[54:55], v[202:203] op_sel_hi:[1,0] neg_lo:[0,1] neg_hi:[0,1]
	v_pk_add_f32 v[52:53], v[52:53], v[202:203] op_sel_hi:[1,0] neg_lo:[0,1] neg_hi:[0,1]
	v_pk_add_f32 v[50:51], v[50:51], v[202:203] op_sel_hi:[1,0] neg_lo:[0,1] neg_hi:[0,1]
	v_pk_add_f32 v[48:49], v[48:49], v[202:203] op_sel_hi:[1,0] neg_lo:[0,1] neg_hi:[0,1]
	s_waitcnt lgkmcnt(0)
	s_nop 0
	v_pk_add_f32 v[46:47], v[46:47], v[202:203] op_sel_hi:[1,0] neg_lo:[0,1] neg_hi:[0,1]
	v_pk_add_f32 v[44:45], v[44:45], v[202:203] op_sel_hi:[1,0] neg_lo:[0,1] neg_hi:[0,1]
	v_pk_add_f32 v[42:43], v[42:43], v[202:203] op_sel_hi:[1,0] neg_lo:[0,1] neg_hi:[0,1]
	v_pk_add_f32 v[40:41], v[40:41], v[202:203] op_sel_hi:[1,0] neg_lo:[0,1] neg_hi:[0,1]
	v_pk_add_f32 v[38:39], v[38:39], v[202:203] op_sel_hi:[1,0] neg_lo:[0,1] neg_hi:[0,1]
	v_pk_add_f32 v[36:37], v[36:37], v[202:203] op_sel_hi:[1,0] neg_lo:[0,1] neg_hi:[0,1]
	v_pk_add_f32 v[34:35], v[34:35], v[202:203] op_sel_hi:[1,0] neg_lo:[0,1] neg_hi:[0,1]
	v_pk_add_f32 v[32:33], v[32:33], v[202:203] op_sel_hi:[1,0] neg_lo:[0,1] neg_hi:[0,1]
.LBB0_775:
	s_waitcnt lgkmcnt(14)
	s_nop 0
	v_mfma_f32_32x32x16_bf16 v[16:31], v[126:129], v[190:193], v[16:31]
	v_exp_f32_e32 v80, v80
	v_exp_f32_e32 v81, v81
	v_exp_f32_e64 v82, v82
	v_exp_f32_e32 v83, v83
	s_waitcnt lgkmcnt(12)
	v_mfma_f32_32x32x16_bf16 v[0:15], v[126:129], v[186:189], v[0:15]
	v_exp_f32_e32 v84, v84
	v_exp_f32_e32 v85, v85
	v_exp_f32_e64 v86, v86
	v_exp_f32_e32 v87, v87
	s_and_b64 vcc, exec, s[4:5]
	v_add_u32_e32 v96, s38, v238
	s_cbranch_vccnz .LBB0_777
	ds_read_b128 v[158:161], v96
	ds_read_b128 v[146:149], v96 offset:512
.LBB0_777:
	s_waitcnt lgkmcnt(10)
	s_nop 0
	v_mfma_f32_32x32x16_bf16 v[16:31], v[122:125], v[182:185], v[16:31]
	v_exp_f32_e32 v88, v88
	v_exp_f32_e32 v89, v89
	v_exp_f32_e32 v90, v90
	v_exp_f32_e32 v91, v91
	s_and_b64 vcc, exec, s[4:5]
	s_cbranch_vccnz .LBB0_779
	ds_read_b128 v[154:157], v96 offset:2048
	ds_read_b128 v[142:145], v96 offset:2560
.LBB0_779:
	s_waitcnt lgkmcnt(8)
	s_nop 0
	v_mfma_f32_32x32x16_bf16 v[0:15], v[122:125], v[178:181], v[0:15]
	v_exp_f32_e32 v92, v92
	v_exp_f32_e32 v93, v93
	v_exp_f32_e32 v94, v94
	v_exp_f32_e32 v95, v95
	s_and_b64 vcc, exec, s[4:5]
	s_cbranch_vccnz .LBB0_781
	ds_read_b128 v[150:153], v96 offset:4096
	ds_read_b128 v[138:141], v96 offset:4608
.LBB0_781:
	s_waitcnt lgkmcnt(6)
	s_nop 0
	v_mfma_f32_32x32x16_bf16 v[16:31], v[118:121], v[174:177], v[16:31]
	v_exp_f32_e32 v64, v64
	v_exp_f32_e32 v65, v65
	v_exp_f32_e32 v66, v66
	v_exp_f32_e32 v67, v67
	s_and_b64 vcc, exec, s[4:5]
	s_cbranch_vccnz .LBB0_783
	ds_read_b128 v[134:137], v96 offset:6144
	ds_read_b128 v[130:133], v96 offset:6656
.LBB0_783:
	s_waitcnt lgkmcnt(4)
	s_nop 0
	v_mfma_f32_32x32x16_bf16 v[0:15], v[118:121], v[170:173], v[0:15]
	v_exp_f32_e32 v68, v68
	v_exp_f32_e32 v69, v69
	v_exp_f32_e64 v70, v70
	v_exp_f32_e32 v71, v71
	s_waitcnt lgkmcnt(2)
	v_mfma_f32_32x32x16_bf16 v[16:31], v[114:117], v[166:169], v[16:31]
	v_exp_f32_e32 v72, v72
	v_exp_f32_e32 v73, v73
	v_exp_f32_e64 v74, v74
	v_exp_f32_e32 v75, v75
	s_waitcnt lgkmcnt(0)
	v_mfma_f32_32x32x16_bf16 v[0:15], v[114:117], v[162:165], v[0:15]
	v_exp_f32_e32 v76, v76
	v_exp_f32_e32 v77, v77
	v_exp_f32_e32 v78, v78
	v_exp_f32_e32 v79, v79
	s_mov_b64 s[4:5], -1
	s_and_b64 vcc, exec, s[16:17]
	s_cbranch_vccz .LBB0_795
	s_and_b64 vcc, exec, s[14:15]
	s_cbranch_vccz .LBB0_786
	s_waitcnt vmcnt(0) lgkmcnt(0)
	s_barrier
	s_mov_b64 s[4:5], 0

.LBB0_790:
	s_waitcnt lgkmcnt(0)
	ds_read_b128 v[162:165], v219 offset:49248
	ds_read_b128 v[166:169], v219 offset:49216
	ds_read_b128 v[170:173], v219 offset:49184
	ds_read_b128 v[174:177], v219 offset:49152
	s_waitcnt lgkmcnt(3)
	s_nop 0
	v_pk_mul_f32 v[30:31], v[30:31], v[164:165]
	s_waitcnt lgkmcnt(2)
	s_nop 0
	v_pk_mul_f32 v[26:27], v[26:27], v[168:169]
	s_waitcnt lgkmcnt(1)
	s_nop 0
	v_pk_mul_f32 v[22:23], v[22:23], v[172:173]
	s_waitcnt lgkmcnt(0)
	s_nop 0
	v_pk_mul_f32 v[18:19], v[18:19], v[176:177]
	v_pk_mul_f32 v[28:29], v[28:29], v[162:163]
	v_pk_mul_f32 v[24:25], v[24:25], v[166:167]
	v_pk_mul_f32 v[20:21], v[20:21], v[170:171]
	v_pk_mul_f32 v[16:17], v[16:17], v[174:175]
	v_pk_mul_f32 v[14:15], v[14:15], v[164:165]
	v_pk_mul_f32 v[10:11], v[10:11], v[168:169]
	v_pk_mul_f32 v[6:7], v[6:7], v[172:173]
	v_pk_mul_f32 v[2:3], v[2:3], v[176:177]
	v_pk_mul_f32 v[12:13], v[12:13], v[162:163]
	v_pk_mul_f32 v[8:9], v[8:9], v[166:167]
	v_pk_mul_f32 v[4:5], v[4:5], v[170:171]
	v_pk_mul_f32 v[0:1], v[0:1], v[174:175]
.LBB0_791:
	s_add_i32 s4, s38, 0x2000
	s_cmpk_lg_i32 s38, 0x4000
	s_cselect_b32 s4, s4, 0
	s_add_i32 s40, s40, 2
	s_nop 0
	s_mov_b64 s[14:15], 0x40000
	v_add_u32_e32 v212, 0x80, v212
	v_lshl_add_u64 v[204:205], v[204:205], 0, s[14:15]
	v_add_u32_e32 v213, 0x200, v213
	s_cmp_lt_u32 s22, s39
	s_nop 0
	s_mov_b64 s[62:63], 0x40000
	v_lshl_add_u64 v[206:207], v[206:207], 0, s[14:15]
	s_cbranch_scc0 .LBB0_744
	s_mov_b32 s22, s46
	s_mov_b32 s46, s4
	s_branch .LBB0_751

.LBB0_797:
	v_max_f32_e32 v80, v80, v80
	v_max_f32_e32 v81, 0, v80
	v_exp_f32_e64 v80, -v81
	s_and_saveexec_b64 s[16:17], s[2:3]
	s_nop 0
	ds_write_b32 v235, v80 offset:49152
	s_or_b64 exec, exec, s[16:17]
	v_sub_f32_e32 v63, v63, v81
	v_sub_f32_e32 v62, v62, v81
	v_sub_f32_e32 v61, v61, v81
	v_sub_f32_e32 v60, v60, v81
	v_sub_f32_e32 v59, v59, v81
	v_sub_f32_e32 v58, v58, v81
	v_sub_f32_e32 v57, v57, v81
	v_sub_f32_e32 v56, v56, v81
	v_sub_f32_e32 v55, v55, v81
	v_sub_f32_e32 v54, v54, v81
	v_sub_f32_e32 v53, v53, v81
	v_sub_f32_e32 v52, v52, v81
	v_sub_f32_e32 v51, v51, v81
	v_sub_f32_e32 v50, v50, v81
	v_sub_f32_e32 v49, v49, v81
	v_sub_f32_e32 v48, v48, v81
	v_sub_f32_e32 v47, v47, v81
	v_sub_f32_e32 v46, v46, v81
	v_sub_f32_e32 v45, v45, v81
	v_sub_f32_e32 v44, v44, v81
	v_sub_f32_e32 v43, v43, v81
	v_sub_f32_e32 v42, v42, v81
	v_sub_f32_e32 v41, v41, v81
	v_sub_f32_e32 v40, v40, v81
	v_sub_f32_e32 v39, v39, v81
	v_sub_f32_e32 v38, v38, v81
	v_sub_f32_e32 v37, v37, v81
	v_sub_f32_e32 v36, v36, v81
	v_sub_f32_e32 v35, v35, v81
	v_sub_f32_e32 v34, v34, v81
	v_sub_f32_e32 v33, v33, v81
	v_sub_f32_e32 v32, v32, v81
	v_add_f32_e32 v202, v202, v81
	v_mul_f32_e32 v96, v96, v80
	s_branch .LBB0_756
.LBB0_800:
	v_max_f32_e32 v96, v96, v96
	v_max_f32_e32 v194, 0, v96
	v_exp_f32_e64 v96, -v194
	s_and_saveexec_b64 s[20:21], s[2:3]
	s_nop 0
	ds_write_b32 v235, v96 offset:49152
	s_or_b64 exec, exec, s[20:21]
	v_sub_f32_e32 v95, v95, v194
	v_sub_f32_e32 v94, v94, v194
	v_sub_f32_e32 v93, v93, v194
	v_sub_f32_e32 v92, v92, v194
	v_sub_f32_e32 v91, v91, v194
	v_sub_f32_e32 v90, v90, v194
	v_sub_f32_e32 v89, v89, v194
	v_sub_f32_e32 v88, v88, v194
	v_sub_f32_e32 v87, v87, v194
	v_sub_f32_e32 v86, v86, v194
	v_sub_f32_e32 v85, v85, v194
	v_sub_f32_e32 v84, v84, v194
	v_sub_f32_e32 v83, v83, v194
	v_sub_f32_e32 v82, v82, v194
	v_sub_f32_e32 v81, v81, v194
	v_sub_f32_e32 v80, v80, v194
	v_sub_f32_e32 v79, v79, v194
	v_sub_f32_e32 v78, v78, v194
	v_sub_f32_e32 v77, v77, v194
	v_sub_f32_e32 v76, v76, v194
	v_sub_f32_e32 v75, v75, v194
	v_sub_f32_e32 v74, v74, v194
	v_sub_f32_e32 v73, v73, v194
	v_sub_f32_e32 v72, v72, v194
	v_sub_f32_e32 v71, v71, v194
	v_sub_f32_e32 v70, v70, v194
	v_sub_f32_e32 v69, v69, v194
	v_sub_f32_e32 v68, v68, v194
	v_sub_f32_e32 v67, v67, v194
	v_sub_f32_e32 v66, v66, v194
	v_sub_f32_e32 v65, v65, v194
	v_sub_f32_e32 v64, v64, v194
	v_add_f32_e32 v202, v202, v194
	v_mul_f32_e32 v240, v240, v96
	s_and_b64 vcc, exec, s[4:5]
	s_cbranch_vccz .LBB0_774
	s_branch .LBB0_775
